# P0 prologue: read-once f32 weight / x row loads marked non-temporal (nt) so they stop evicting the freshly written int8 operands; no arithmetic change
# speedup vs baseline: 1.0304x; 1.0158x over previous
; #define P0_LOAD(T, V) do { _Pragma("unroll") for (int i = 0; i < 8; ++i) V[i] = *(const GAS f32x4*)(T.src + (size_t)(i * 8 + (F.lane >> 3)) * T.N + (F.lane & 7) * 4); } while (0)
; __device__ __forceinline__ void p0_prologue(Frame& F) {
;     ...
;     {
;         int it = gw; TItem ta, tb; f32x4 va[8], vb[8];
;         if (it < NITEMS) {
;             ta = decode(it); P0_LOAD(ta, va);
.LBB0_28:
	v_lshrrev_b32_e32 v66, 3, v202
	v_lshlrev_b32_e32 v1, 2, v0
	v_and_b32_e32 v68, 28, v1
	v_mul_u32_u24_e32 v1, s26, v66
	v_or_b32_e32 v72, 8, v66
	v_lshlrev_b32_e32 v2, 2, v1
	v_mul_u32_u24_e32 v1, s26, v72
	v_or_b32_e32 v74, 16, v66
	v_lshlrev_b32_e32 v4, 2, v1
	v_mul_u32_u24_e32 v1, s26, v74
	v_or_b32_e32 v76, 24, v66
	v_lshlrev_b32_e32 v10, 2, v1
	v_mul_u32_u24_e32 v1, s26, v76
	v_lshlrev_b32_e32 v12, 2, v1
	v_or_b32_e32 v1, 32, v66
	v_or_b32_e32 v67, 40, v66
	v_or_b32_e32 v69, 48, v66
	v_or_b32_e32 v73, 56, v66
	v_mov_b32_e32 v71, 0
	v_lshlrev_b32_e32 v70, 2, v68
	v_mul_u32_u24_e32 v18, s26, v1
	v_mul_u32_u24_e32 v20, s26, v67
	v_mul_u32_u24_e32 v28, s26, v69
	v_mul_u32_u24_e32 v30, s26, v73
	v_lshl_add_u64 v[26:27], s[24:25], 0, v[70:71]
	v_mov_b32_e32 v3, v71
	v_mov_b32_e32 v5, v71
	v_mov_b32_e32 v11, v71
	v_mov_b32_e32 v13, v71
	v_lshlrev_b32_e32 v18, 2, v18
	v_mov_b32_e32 v19, v71
	v_lshlrev_b32_e32 v20, 2, v20
	v_mov_b32_e32 v21, v71
	v_lshlrev_b32_e32 v28, 2, v28
	v_mov_b32_e32 v29, v71
	v_lshlrev_b32_e32 v30, 2, v30
	v_mov_b32_e32 v31, v71
	v_lshl_add_u64 v[2:3], v[26:27], 0, v[2:3]
	v_lshl_add_u64 v[4:5], v[26:27], 0, v[4:5]
	v_lshl_add_u64 v[10:11], v[26:27], 0, v[10:11]
	v_lshl_add_u64 v[12:13], v[26:27], 0, v[12:13]
	v_lshl_add_u64 v[18:19], v[26:27], 0, v[18:19]
	v_lshl_add_u64 v[20:21], v[26:27], 0, v[20:21]
	v_lshl_add_u64 v[28:29], v[26:27], 0, v[28:29]
	v_lshl_add_u64 v[26:27], v[26:27], 0, v[30:31]
	global_load_dwordx4 v[6:9], v[2:3], off nt
	s_nop 0
	global_load_dwordx4 v[2:5], v[4:5], off nt
	s_nop 0
	global_load_dwordx4 v[14:17], v[10:11], off nt
	s_nop 0
	global_load_dwordx4 v[10:13], v[12:13], off nt
	s_nop 0
	global_load_dwordx4 v[22:25], v[18:19], off nt
	s_nop 0
	global_load_dwordx4 v[18:21], v[20:21], off nt
	s_nop 0
	global_load_dwordx4 v[30:33], v[28:29], off nt
	s_nop 0
	global_load_dwordx4 v[26:29], v[26:27], off nt
	v_readlane_b32 s24, v255, 10
	v_lshlrev_b32_e32 v36, 4, v0
	s_lshl_b32 s24, s24, 14
	v_and_b32_e32 v78, 48, v36
	s_add_i32 s24, s24, 0
	v_mul_u32_u24_e32 v36, 0x84, v78
	v_and_b32_e32 v37, 60, v202
	s_add_u32 s43, s66, 0xa800000
	v_add3_u32 v75, s24, v36, v37
	v_and_b32_e32 v36, 7, v0
	s_addc_u32 s44, s67, 0
	v_mul_u32_u24_e32 v37, 0x420, v36
	v_lshlrev_b32_e32 v38, 2, v66
	s_add_u32 s45, s66, 0x9700000
	v_add_u32_e32 v34, s24, v70
	v_mul_u32_u24_e32 v35, 0x84, v66
	v_add3_u32 v77, s24, v37, v38
	v_readlane_b32 s24, v255, 2
	v_lshrrev_b32_e32 v82, 2, v202
	s_mov_b32 s25, 0
	s_addc_u32 s46, s67, 0
	v_mov_b32_e32 v79, v71
	v_lshlrev_b32_e32 v80, 4, v36
	v_mov_b32_e32 v81, v71
	s_lshl_b32 s47, s24, 4
	s_movk_i32 s48, 0xff81
	s_mov_b32 s49, 0xc0c0500
	s_movk_i32 s50, 0x7fff
	s_mov_b32 s51, 0xffff0000
	v_add_u32_e32 v83, v34, v35
	v_mov_b32_e32 v85, 0x7f
	s_mov_b32 s71, s6
	v_or_b32_e32 v84, 16, v82
	s_branch .LBB0_31

; #define P0_LOAD(T, V) do { _Pragma("unroll") for (int i = 0; i < 8; ++i) V[i] = *(const GAS f32x4*)(T.src + (size_t)(i * 8 + (F.lane >> 3)) * T.N + (F.lane & 7) * 4); } while (0)
; __device__ __forceinline__ void p0_prologue(Frame& F) {
;     ...
;                 { const int itn = it + NGW; tb = decode(itn < NITEMS ? itn : gw); P0_LOAD(tb, vb); }
;                 P0_PROC(ta, va); it += NGW; if (it >= NITEMS) break;
.LBB0_49:
	v_lshlrev_b32_e32 v70, 2, v68
	s_waitcnt vmcnt(7)
	v_mul_u32_u24_e32 v34, s38, v66
	v_mul_u32_u24_e32 v36, s38, v72
	s_waitcnt vmcnt(5)
	v_mul_u32_u24_e32 v42, s38, v74
	v_mul_u32_u24_e32 v44, s38, v76
	s_waitcnt vmcnt(1)
	v_mul_u32_u24_e32 v52, s38, v1
	v_mul_u32_u24_e32 v54, s38, v67
	v_mul_u32_u24_e32 v56, s38, v69
	v_mul_u32_u24_e32 v58, s38, v73
	v_lshl_add_u64 v[50:51], s[36:37], 0, v[70:71]
	v_lshlrev_b32_e32 v34, 2, v34
	v_mov_b32_e32 v35, v71
	v_lshlrev_b32_e32 v36, 2, v36
	v_mov_b32_e32 v37, v71
	v_lshlrev_b32_e32 v42, 2, v42
	v_mov_b32_e32 v43, v71
	v_lshlrev_b32_e32 v44, 2, v44
	v_mov_b32_e32 v45, v71
	v_lshlrev_b32_e32 v52, 2, v52
	v_mov_b32_e32 v53, v71
	v_lshlrev_b32_e32 v54, 2, v54
	v_mov_b32_e32 v55, v71
	v_lshlrev_b32_e32 v56, 2, v56
	v_mov_b32_e32 v57, v71
	v_lshlrev_b32_e32 v58, 2, v58
	v_mov_b32_e32 v59, v71
	v_lshl_add_u64 v[34:35], v[50:51], 0, v[34:35]
	v_lshl_add_u64 v[36:37], v[50:51], 0, v[36:37]
	v_lshl_add_u64 v[42:43], v[50:51], 0, v[42:43]
	v_lshl_add_u64 v[44:45], v[50:51], 0, v[44:45]
	v_lshl_add_u64 v[52:53], v[50:51], 0, v[52:53]
	v_lshl_add_u64 v[54:55], v[50:51], 0, v[54:55]
	v_lshl_add_u64 v[56:57], v[50:51], 0, v[56:57]
	v_lshl_add_u64 v[50:51], v[50:51], 0, v[58:59]
	global_load_dwordx4 v[38:41], v[34:35], off nt
	s_nop 0
	global_load_dwordx4 v[34:37], v[36:37], off nt
	s_nop 0
	global_load_dwordx4 v[46:49], v[42:43], off nt
	s_nop 0
	global_load_dwordx4 v[42:45], v[44:45], off nt
	s_nop 0
	global_load_dwordx4 v[62:65], v[52:53], off nt
	global_load_dwordx4 v[58:61], v[54:55], off nt
	s_nop 0
	global_load_dwordx4 v[54:57], v[56:57], off nt
	s_nop 0
	global_load_dwordx4 v[50:53], v[50:51], off nt
	v_add_u32_e32 v86, 0x420, v83
	v_add_u32_e32 v87, 0x428, v83
	v_add_u32_e32 v88, 0x840, v83
	v_add_u32_e32 v89, 0x848, v83
	v_add_u32_e32 v90, 0xc60, v83
	v_add_u32_e32 v91, 0xc68, v83
	v_add_u32_e32 v92, 0x1080, v83
	v_add_u32_e32 v93, 0x1088, v83
	v_add_u32_e32 v94, 0x14a0, v83
	v_add_u32_e32 v95, 0x14a8, v83
	v_add_u32_e32 v96, 0x18c0, v83
	v_add_u32_e32 v97, 0x18c8, v83
	v_add_u32_e32 v98, 0x1ce0, v83
	v_add_u32_e32 v99, 0x1ce8, v83
	s_waitcnt vmcnt(15)
	ds_write2_b32 v83, v6, v7 offset1:1
	ds_write2_b32 v83, v8, v9 offset0:2 offset1:3
	s_waitcnt vmcnt(14)
	ds_write2_b32 v86, v2, v3 offset1:1
	ds_write2_b32 v87, v4, v5 offset1:1
	s_waitcnt vmcnt(13)
	ds_write2_b32 v88, v14, v15 offset1:1
	ds_write2_b32 v89, v16, v17 offset1:1
	s_waitcnt vmcnt(12)
	ds_write2_b32 v90, v10, v11 offset1:1
	ds_write2_b32 v91, v12, v13 offset1:1
	s_waitcnt vmcnt(11)
	ds_write2_b32 v92, v22, v23 offset1:1
	ds_write2_b32 v93, v24, v25 offset1:1
	s_waitcnt vmcnt(10)
	ds_write2_b32 v94, v18, v19 offset1:1
	ds_write2_b32 v95, v20, v21 offset1:1
	s_waitcnt vmcnt(9)
	ds_write2_b32 v96, v30, v31 offset1:1
	ds_write2_b32 v97, v32, v33 offset1:1
	s_waitcnt vmcnt(8)
	ds_write2_b32 v98, v26, v27 offset1:1
	ds_write2_b32 v99, v28, v29 offset1:1
	s_waitcnt lgkmcnt(0)
	s_mov_b64 s[36:37], -1
	s_cmp_eq_u32 s70, 0
	s_cbranch_scc1 .LBB0_75
	ds_read2_b32 v[2:3], v75 offset1:33
	s_cmp_lg_u32 s70, 2
	s_cselect_b64 s[36:37], -1, 0
	s_mov_b64 s[38:39], -1
	s_and_b64 vcc, exec, s[36:37]
	s_waitcnt lgkmcnt(0)
	v_mul_f32_e32 v7, s41, v2
	v_mul_f32_e32 v6, s41, v3
	s_cbranch_vccz .LBB0_52
	ds_read2_b32 v[4:5], v75 offset0:66 offset1:99
	ds_read2_b32 v[8:9], v75 offset0:132 offset1:165
	v_mov_b32_e32 v2, v71
	v_mov_b32_e32 v3, v71
	v_add_u32_e32 v12, 0x400, v75
	s_waitcnt lgkmcnt(1)
	v_mul_f32_e32 v10, s41, v4
	v_mul_f32_e32 v11, s41, v5
	s_waitcnt lgkmcnt(0)
	v_mul_f32_e32 v8, s41, v8
	v_mul_f32_e32 v9, s41, v9
	ds_read2_b32 v[4:5], v75 offset0:198 offset1:231
	v_cvt_pk_fp8_f32 v2, v7, v6
	v_cvt_pk_fp8_f32 v3, v8, v9
	ds_read2_b32 v[8:9], v12 offset0:8 offset1:41
	s_mov_b64 s[38:39], 0
	v_cvt_pk_fp8_f32 v2, v10, v11 op_sel:[0,0,1]
	s_waitcnt lgkmcnt(1)
	v_mul_f32_e32 v4, s41, v4
	v_mul_f32_e32 v5, s41, v5
	ds_read2_b32 v[10:11], v12 offset0:74 offset1:107
	v_cvt_pk_fp8_f32 v3, v4, v5 op_sel:[0,0,1]
	s_waitcnt lgkmcnt(1)
	v_mul_f32_e32 v5, s41, v8
	v_mul_f32_e32 v13, s41, v9
	ds_read2_b32 v[8:9], v12 offset0:140 offset1:173
	v_mov_b32_e32 v4, v71
	v_cvt_pk_fp8_f32 v4, v5, v13
	s_waitcnt lgkmcnt(1)
	v_mul_f32_e32 v13, s41, v10
	v_mul_f32_e32 v14, s41, v11
	ds_read2_b32 v[10:11], v12 offset0:206 offset1:239
	s_waitcnt lgkmcnt(1)
	v_mul_f32_e32 v8, s41, v8
	v_mul_f32_e32 v9, s41, v9
	v_mov_b32_e32 v5, v71
	v_cvt_pk_fp8_f32 v5, v8, v9
	s_waitcnt lgkmcnt(0)
	v_mul_f32_e32 v8, s41, v10
	v_mul_f32_e32 v9, s41, v11
	v_cvt_pk_fp8_f32 v4, v13, v14 op_sel:[0,0,1]
	v_cvt_pk_fp8_f32 v5, v8, v9 op_sel:[0,0,1]

; #define P0_LOAD(T, V) do { _Pragma("unroll") for (int i = 0; i < 8; ++i) V[i] = *(const GAS f32x4*)(T.src + (size_t)(i * 8 + (F.lane >> 3)) * T.N + (F.lane & 7) * 4); } while (0)
; __device__ __forceinline__ void p0_prologue(Frame& F) {
;     ...
;                 { const int itn = it + NGW; ta = decode(itn < NITEMS ? itn : gw); P0_LOAD(ta, va); }
;                 P0_PROC(tb, vb); it += NGW; if (it >= NITEMS) break;
.LBB0_79:
	v_mul_u32_u24_e32 v2, s38, v66
	v_lshl_add_u64 v[26:27], s[36:37], 0, v[70:71]
	v_lshlrev_b32_e32 v70, 2, v2
	v_mul_u32_u24_e32 v4, s38, v72
	v_lshl_add_u64 v[2:3], v[26:27], 0, v[70:71]
	v_lshlrev_b32_e32 v70, 2, v4
	v_mul_u32_u24_e32 v10, s38, v74
	v_lshl_add_u64 v[4:5], v[26:27], 0, v[70:71]
	v_lshlrev_b32_e32 v70, 2, v10
	v_mul_u32_u24_e32 v12, s38, v76
	v_lshl_add_u64 v[10:11], v[26:27], 0, v[70:71]
	v_lshlrev_b32_e32 v70, 2, v12
	v_mul_u32_u24_e32 v18, s38, v1
	v_lshl_add_u64 v[12:13], v[26:27], 0, v[70:71]
	v_lshlrev_b32_e32 v70, 2, v18
	v_mul_u32_u24_e32 v20, s38, v67
	v_lshl_add_u64 v[18:19], v[26:27], 0, v[70:71]
	v_lshlrev_b32_e32 v70, 2, v20
	v_mul_u32_u24_e32 v28, s38, v69
	v_lshl_add_u64 v[20:21], v[26:27], 0, v[70:71]
	v_lshlrev_b32_e32 v70, 2, v28
	v_mul_u32_u24_e32 v30, s38, v73
	v_lshl_add_u64 v[28:29], v[26:27], 0, v[70:71]
	v_lshlrev_b32_e32 v70, 2, v30
	v_lshl_add_u64 v[26:27], v[26:27], 0, v[70:71]
	global_load_dwordx4 v[6:9], v[2:3], off nt
	s_nop 0
	global_load_dwordx4 v[2:5], v[4:5], off nt
	s_nop 0
	global_load_dwordx4 v[14:17], v[10:11], off nt
	s_nop 0
	global_load_dwordx4 v[10:13], v[12:13], off nt
	s_nop 0
	global_load_dwordx4 v[22:25], v[18:19], off nt
	s_nop 0
	global_load_dwordx4 v[18:21], v[20:21], off nt
	s_nop 0
	global_load_dwordx4 v[30:33], v[28:29], off nt
	s_nop 0
	global_load_dwordx4 v[26:29], v[26:27], off nt
	s_waitcnt vmcnt(16)
	ds_write2_b32 v83, v38, v39 offset1:1
	ds_write2_b32 v83, v40, v41 offset0:2 offset1:3
	s_waitcnt vmcnt(15)
	ds_write2_b32 v86, v34, v35 offset1:1
	ds_write2_b32 v87, v36, v37 offset1:1
	s_waitcnt vmcnt(14)
	ds_write2_b32 v88, v46, v47 offset1:1
	ds_write2_b32 v89, v48, v49 offset1:1
	s_waitcnt vmcnt(13)
	ds_write2_b32 v90, v42, v43 offset1:1
	ds_write2_b32 v91, v44, v45 offset1:1
	s_waitcnt vmcnt(12)
	ds_write2_b32 v92, v62, v63 offset1:1
	ds_write2_b32 v93, v64, v65 offset1:1
	s_waitcnt vmcnt(11)
	ds_write2_b32 v94, v58, v59 offset1:1
	ds_write2_b32 v95, v60, v61 offset1:1
	s_waitcnt vmcnt(10)
	ds_write2_b32 v96, v54, v55 offset1:1
	ds_write2_b32 v97, v56, v57 offset1:1
	s_waitcnt vmcnt(9)
	ds_write2_b32 v98, v50, v51 offset1:1
	ds_write2_b32 v99, v52, v53 offset1:1
	s_waitcnt lgkmcnt(0)
	s_xor_b64 s[34:35], s[34:35], -1
	s_andn2_b64 vcc, exec, s[34:35]
	s_mov_b64 s[34:35], -1
	s_cbranch_vccnz .LBB0_89
	ds_read2_b32 v[34:35], v75 offset1:33
	s_xor_b64 s[30:31], s[30:31], -1
	s_and_b64 vcc, exec, s[30:31]
	v_add_u32_e32 v38, 0x400, v75
	s_waitcnt lgkmcnt(0)
	v_mul_f32_e32 v40, s69, v34
	v_mul_f32_e32 v39, s69, v35
	s_cbranch_vccz .LBB0_82
	ds_read2_b32 v[36:37], v75 offset0:66 offset1:99
	ds_read2_b32 v[42:43], v75 offset0:132 offset1:165
	v_mov_b32_e32 v34, v71
	v_mov_b32_e32 v35, v71
	v_cvt_pk_fp8_f32 v34, v40, v39
	s_waitcnt lgkmcnt(1)
	v_mul_f32_e32 v41, s69, v36
	v_mul_f32_e32 v44, s69, v37
	s_waitcnt lgkmcnt(0)
	v_mul_f32_e32 v42, s69, v42
	v_mul_f32_e32 v43, s69, v43
	ds_read2_b32 v[36:37], v75 offset0:198 offset1:231
	v_cvt_pk_fp8_f32 v35, v42, v43
	ds_read2_b32 v[42:43], v38 offset0:8 offset1:41
	v_cvt_pk_fp8_f32 v34, v41, v44 op_sel:[0,0,1]
	ds_read2_b32 v[44:45], v38 offset0:74 offset1:107
	s_waitcnt lgkmcnt(2)
	v_mul_f32_e32 v36, s69, v36
	v_mul_f32_e32 v37, s69, v37
	v_cvt_pk_fp8_f32 v35, v36, v37 op_sel:[0,0,1]
	s_waitcnt lgkmcnt(1)
	v_mul_f32_e32 v37, s69, v42
	v_mul_f32_e32 v41, s69, v43
	ds_read2_b32 v[42:43], v38 offset0:140 offset1:173
	v_mov_b32_e32 v36, v71
	v_cvt_pk_fp8_f32 v36, v37, v41
	s_waitcnt lgkmcnt(1)
	v_mul_f32_e32 v41, s69, v44
	v_mul_f32_e32 v46, s69, v45
	ds_read2_b32 v[44:45], v38 offset0:206 offset1:239
	s_waitcnt lgkmcnt(1)
	v_mul_f32_e32 v42, s69, v42
	v_mul_f32_e32 v43, s69, v43
	v_mov_b32_e32 v37, v71
	v_cvt_pk_fp8_f32 v37, v42, v43
	v_cvt_pk_fp8_f32 v36, v41, v46 op_sel:[0,0,1]
	s_waitcnt lgkmcnt(0)
	v_mul_f32_e32 v41, s69, v44
	v_mul_f32_e32 v42, s69, v45
	v_cvt_pk_fp8_f32 v37, v41, v42 op_sel:[0,0,1]
	s_mov_b64 s[34:35], 0

; #define GAS __attribute__((address_space(1)))
; #define HN_LOAD(V, M) do { const GAS f32x4* xr_ = (const GAS f32x4*)(F.in[I_X] + (size_t)(M) * DM) + F.lane; _Pragma("unroll") for (int i = 0; i < 16; ++i) V[i] = xr_[64 * i]; } while (0)
; __device__ __forceinline__ void p0_prologue(Frame& F) {
;     ...
;     {
;         const GAS f32x4* gr = (const GAS f32x4*)F.in[I_NMIX] + F.lane; f32x4 gq[16];
; #pragma unroll
;         for (int i = 0; i < 16; ++i) gq[i] = gr[64 * i];
;     ...
;         int m = gw;
;         if (m < T_) {
;             f32x4 va[16], vb[16]; HN_LOAD(va, m);
.LBB0_92:
	s_cmpk_gt_i32 s6, 0x1fff
	s_cbranch_scc1 .LBB0_97
	v_lshlrev_b32_e32 v78, 4, v202
	v_mov_b32_e32 v79, 0
	s_waitcnt vmcnt(7)
	v_lshl_add_u64 v[34:35], s[10:11], 0, v[78:79]
	s_waitcnt vmcnt(3)
	v_add_co_u32_e32 v18, vcc, 0x3000, v34
	s_ashr_i32 s7, s6, 31
	s_nop 0
	v_addc_co_u32_e32 v19, vcc, 0, v35, vcc
	v_add_co_u32_e32 v36, vcc, 0x2000, v34
	s_lshl_b64 s[0:1], s[6:7], 14
	s_nop 0
	v_addc_co_u32_e32 v37, vcc, 0, v35, vcc
	v_add_co_u32_e32 v66, vcc, 0x1000, v34
	s_add_u32 s0, s8, s0
	s_nop 0
	v_addc_co_u32_e32 v67, vcc, 0, v35, vcc
	s_addc_u32 s1, s9, s1
	global_load_dwordx4 v[2:5], v[18:19], off offset:3072 nt
	global_load_dwordx4 v[6:9], v[18:19], off offset:2048 nt
	global_load_dwordx4 v[10:13], v[18:19], off offset:1024 nt
	global_load_dwordx4 v[14:17], v[18:19], off nt
	s_nop 0
	global_load_dwordx4 v[18:21], v[36:37], off offset:3072 nt
	global_load_dwordx4 v[22:25], v[36:37], off offset:2048 nt
	global_load_dwordx4 v[26:29], v[36:37], off offset:1024 nt
	global_load_dwordx4 v[30:33], v[36:37], off nt
	s_movk_i32 s18, 0x1000
	global_load_dwordx4 v[34:37], v[66:67], off offset:3072 nt
	global_load_dwordx4 v[38:41], v[66:67], off offset:2048 nt
	global_load_dwordx4 v[42:45], v[66:67], off offset:1024 nt
	global_load_dwordx4 v[46:49], v[66:67], off nt
	global_load_dwordx4 v[50:53], v78, s[10:11] offset:3072
	global_load_dwordx4 v[54:57], v78, s[10:11] offset:2048
	global_load_dwordx4 v[58:61], v78, s[10:11] offset:1024
	global_load_dwordx4 v[62:65], v78, s[10:11]
	v_lshl_add_u64 v[66:67], s[0:1], 0, v[78:79]
	v_add_co_u32_e32 v68, vcc, s18, v66
	s_movk_i32 s13, 0x2000
	s_nop 0
	v_addc_co_u32_e32 v69, vcc, 0, v67, vcc
	v_add_co_u32_e32 v70, vcc, s13, v66
	s_movk_i32 s12, 0x3000
	s_nop 0
	v_addc_co_u32_e32 v71, vcc, 0, v67, vcc
	v_add_co_u32_e32 v66, vcc, s12, v66
	global_load_dwordx4 v[190:193], v78, s[0:1]
	global_load_dwordx4 v[186:189], v78, s[0:1] offset:1024
	global_load_dwordx4 v[182:185], v78, s[0:1] offset:2048
	global_load_dwordx4 v[178:181], v78, s[0:1] offset:3072
	global_load_dwordx4 v[170:173], v[68:69], off offset:1024 nt
	global_load_dwordx4 v[162:165], v[68:69], off offset:2048 nt
	global_load_dwordx4 v[174:177], v[70:71], off offset:-4096 nt
	global_load_dwordx4 v[158:161], v[70:71], off nt
	global_load_dwordx4 v[154:157], v[70:71], off offset:1024 nt
	global_load_dwordx4 v[150:153], v[70:71], off offset:2048 nt
	global_load_dwordx4 v[110:113], v[70:71], off offset:3072 nt
	v_addc_co_u32_e32 v67, vcc, 0, v67, vcc
	global_load_dwordx4 v[166:169], v[68:69], off offset:3072 nt
	global_load_dwordx4 v[102:105], v[66:67], off nt
	global_load_dwordx4 v[74:77], v[66:67], off offset:1024 nt
	global_load_dwordx4 v[70:73], v[66:67], off offset:2048 nt
	s_nop 0
	global_load_dwordx4 v[66:69], v[66:67], off offset:3072 nt
	v_lshl_add_u64 v[194:195], s[8:9], 0, v[78:79]
	v_lshlrev_b32_e32 v78, 2, v202
	v_lshl_add_u64 v[78:79], s[66:67], 0, v[78:79]
	s_mov_b64 s[0:1], 0x6d00000
	v_lshl_add_u64 v[196:197], v[78:79], 0, s[0:1]
	v_readlane_b32 s0, v255, 2
	s_lshl_b32 s7, s0, 4
	v_mov_b32_e32 v1, 0x358637bd
	s_mov_b32 s10, 0xf800000
	v_mov_b32_e32 v200, 0x260
	s_movk_i32 s11, 0xff81
	s_mov_b32 s19, 0x40c0c00
	v_mov_b32_e32 v201, 0x1080
	v_mov_b32_e32 v204, 0x7f
	s_mov_b32 s21, s6
	s_branch .LBB0_95

; #define HN_LOAD(V, M) do { const GAS f32x4* xr_ = (const GAS f32x4*)(F.in[I_X] + (size_t)(M) * DM) + F.lane; _Pragma("unroll") for (int i = 0; i < 16; ++i) V[i] = xr_[64 * i]; } while (0)
; __device__ __forceinline__ void p0_prologue(Frame& F) {
;     ...
;         int m = gw;
;         if (m < T_) {
;             f32x4 va[16], vb[16]; HN_LOAD(va, m);
;             for (;;) {
;                 { const int mn = m + NGW; HN_LOAD(vb, mn < T_ ? mn : gw); }
;                 HN_PROC(va, m); m += NGW; if (m >= T_) break;
;                 { const int mn = m + NGW; HN_LOAD(va, mn < T_ ? mn : gw); }
;                 HN_PROC(vb, m); m += NGW; if (m >= T_) break;
.LBB0_95:
	s_waitcnt vmcnt(15)
	v_mul_f32_e32 v82, v191, v191
	v_mul_f32_e32 v83, v193, v193
	v_fmac_f32_e32 v82, v190, v190
	v_fmac_f32_e32 v83, v192, v192
	v_add_f32_e32 v82, v82, v83
	s_waitcnt vmcnt(14)
	v_mul_f32_e32 v83, v187, v187
	v_mul_f32_e32 v84, v189, v189
	v_fmac_f32_e32 v83, v186, v186
	v_fmac_f32_e32 v84, v188, v188
	v_add_f32_e32 v83, v83, v84
	v_add_f32_e32 v82, v82, v83
	s_waitcnt vmcnt(13)
	v_mul_f32_e32 v83, v183, v183
	v_mul_f32_e32 v84, v185, v185
	v_fmac_f32_e32 v83, v182, v182
	v_fmac_f32_e32 v84, v184, v184
	v_add_f32_e32 v83, v83, v84
	v_add_f32_e32 v82, v82, v83
	s_waitcnt vmcnt(12)
	v_mul_f32_e32 v83, v179, v179
	v_mul_f32_e32 v84, v181, v181
	v_fmac_f32_e32 v83, v178, v178
	v_fmac_f32_e32 v84, v180, v180
	v_add_f32_e32 v83, v83, v84
	v_add_f32_e32 v82, v82, v83
	s_waitcnt vmcnt(9)
	v_mul_f32_e32 v83, v175, v175
	v_mul_f32_e32 v84, v177, v177
	v_fmac_f32_e32 v83, v174, v174
	v_fmac_f32_e32 v84, v176, v176
	v_add_f32_e32 v83, v83, v84
	v_add_f32_e32 v82, v82, v83
	v_mul_f32_e32 v83, v171, v171
	v_mul_f32_e32 v84, v173, v173
	v_fmac_f32_e32 v83, v170, v170
	v_fmac_f32_e32 v84, v172, v172
	v_add_f32_e32 v83, v83, v84
	v_add_f32_e32 v82, v82, v83
	v_mul_f32_e32 v83, v163, v163
	v_mul_f32_e32 v84, v165, v165
	v_fmac_f32_e32 v83, v162, v162
	v_fmac_f32_e32 v84, v164, v164
	v_add_f32_e32 v83, v83, v84
	v_add_f32_e32 v82, v82, v83
	s_waitcnt vmcnt(4)
	v_mul_f32_e32 v83, v167, v167
	v_mul_f32_e32 v84, v169, v169
	v_fmac_f32_e32 v83, v166, v166
	v_fmac_f32_e32 v84, v168, v168
	v_add_f32_e32 v83, v83, v84
	v_add_f32_e32 v82, v82, v83
	v_mul_f32_e32 v83, v159, v159
	v_mul_f32_e32 v84, v161, v161
	v_fmac_f32_e32 v83, v158, v158
	v_fmac_f32_e32 v84, v160, v160
	v_add_f32_e32 v83, v83, v84
	v_add_f32_e32 v82, v82, v83
	v_mul_f32_e32 v83, v155, v155
	v_mul_f32_e32 v84, v157, v157
	v_fmac_f32_e32 v83, v154, v154
	v_fmac_f32_e32 v84, v156, v156
	v_add_f32_e32 v83, v83, v84
	v_add_f32_e32 v82, v82, v83
	v_mul_f32_e32 v83, v151, v151
	v_mul_f32_e32 v84, v153, v153
	v_fmac_f32_e32 v83, v150, v150
	v_fmac_f32_e32 v84, v152, v152
	v_add_f32_e32 v83, v83, v84
	v_add_f32_e32 v82, v82, v83
	v_mul_f32_e32 v83, v111, v111
	v_mul_f32_e32 v84, v113, v113
	v_fmac_f32_e32 v83, v110, v110
	v_fmac_f32_e32 v84, v112, v112
	v_add_f32_e32 v83, v83, v84
	v_add_f32_e32 v82, v82, v83
	s_waitcnt vmcnt(3)
	v_mul_f32_e32 v83, v103, v103
	v_mul_f32_e32 v84, v105, v105
	v_fmac_f32_e32 v83, v102, v102
	v_fmac_f32_e32 v84, v104, v104
	v_add_f32_e32 v83, v83, v84
	v_add_f32_e32 v82, v82, v83
	s_waitcnt vmcnt(2)
	v_mul_f32_e32 v83, v75, v75
	v_mul_f32_e32 v84, v77, v77
	v_fmac_f32_e32 v83, v74, v74
	v_fmac_f32_e32 v84, v76, v76
	v_add_f32_e32 v83, v83, v84
	v_add_f32_e32 v82, v82, v83
	s_waitcnt vmcnt(1)
	v_mul_f32_e32 v83, v71, v71
	v_mul_f32_e32 v84, v73, v73
	s_add_i32 s20, s21, s33
	v_fmac_f32_e32 v83, v70, v70
	v_fmac_f32_e32 v84, v72, v72
	s_cmpk_lt_i32 s20, 0x2000
	v_add_f32_e32 v83, v83, v84
	s_cselect_b32 s0, s20, s6
	v_add_f32_e32 v82, v82, v83
	s_waitcnt vmcnt(0)
	v_mul_f32_e32 v83, v67, v67
	v_mul_f32_e32 v84, v69, v69
	s_ashr_i32 s1, s0, 31
	v_fmac_f32_e32 v83, v66, v66
	v_fmac_f32_e32 v84, v68, v68
	s_lshl_b64 s[0:1], s[0:1], 14
	v_add_f32_e32 v83, v83, v84
	v_lshl_add_u64 v[78:79], v[194:195], 0, s[0:1]
	v_add_f32_e32 v82, v82, v83
	v_add_co_u32_e32 v80, vcc, s18, v78
	s_nop 0
	v_add_f32_dpp v82, v82, v82 quad_perm:[1,0,3,2] row_mask:0xf bank_mask:0xf bound_ctrl:1
	v_addc_co_u32_e32 v81, vcc, 0, v79, vcc
	s_nop 0
	v_add_f32_dpp v82, v82, v82 quad_perm:[2,3,0,1] row_mask:0xf bank_mask:0xf bound_ctrl:1
	v_add_co_u32_e32 v138, vcc, s13, v78
	s_nop 0
	v_add_f32_dpp v82, v82, v82 row_half_mirror row_mask:0xf bank_mask:0xf bound_ctrl:1
	v_addc_co_u32_e32 v139, vcc, 0, v79, vcc
	s_nop 0
	v_add_f32_dpp v205, v82, v82 row_mirror row_mask:0xf bank_mask:0xf bound_ctrl:1
	v_add_co_u32_e32 v198, vcc, s12, v78
	v_mov_b32_e32 v206, v205
	global_load_dwordx4 v[134:137], v[78:79], off nt
	global_load_dwordx4 v[126:129], v[78:79], off offset:1024 nt
	v_addc_co_u32_e32 v199, vcc, 0, v79, vcc
	global_load_dwordx4 v[146:149], v[78:79], off offset:2048 nt
	global_load_dwordx4 v[142:145], v[78:79], off offset:3072 nt
	global_load_dwordx4 v[114:117], v[138:139], off nt
	global_load_dwordx4 v[106:109], v[138:139], off offset:1024 nt
	global_load_dwordx4 v[98:101], v[138:139], off offset:2048 nt
	global_load_dwordx4 v[94:97], v[138:139], off offset:3072 nt
	global_load_dwordx4 v[130:133], v[80:81], off offset:1024 nt
	global_load_dwordx4 v[122:125], v[80:81], off offset:2048 nt
	global_load_dwordx4 v[118:121], v[80:81], off offset:3072 nt
	global_load_dwordx4 v[90:93], v[198:199], off nt
	global_load_dwordx4 v[86:89], v[198:199], off offset:1024 nt
	global_load_dwordx4 v[82:85], v[198:199], off offset:2048 nt
	s_nop 0
	global_load_dwordx4 v[138:141], v[138:139], off offset:-4096 nt
	s_nop 0
	global_load_dwordx4 v[78:81], v[198:199], off offset:3072 nt
	s_cmpk_gt_i32 s20, 0x1fff
	v_permlane16_swap_b32_e32 v205, v206
	v_add_f32_e32 v198, v205, v206
	v_mov_b32_e32 v199, v198
	s_nop 1
	v_permlane32_swap_b32_e32 v198, v199
	v_add_f32_e32 v198, v198, v199
	v_fmamk_f32 v198, v198, 0x39800000, v1
	v_mul_f32_e32 v199, 0x4f800000, v198
	v_cmp_gt_f32_e32 vcc, s10, v198
	s_nop 1
	v_cndmask_b32_e32 v198, v198, v199, vcc
	v_sqrt_f32_e32 v199, v198
	s_nop 0
	v_add_u32_e32 v205, -1, v199
	v_fma_f32 v206, -v205, v199, v198
	v_cmp_ge_f32_e64 s[0:1], 0, v206
	v_add_u32_e32 v206, 1, v199
	s_nop 0
	v_cndmask_b32_e64 v205, v199, v205, s[0:1]
	v_fma_f32 v199, -v206, v199, v198
	v_cmp_lt_f32_e64 s[0:1], 0, v199
	s_nop 1
	v_cndmask_b32_e64 v199, v205, v206, s[0:1]
	v_mul_f32_e32 v205, 0x37800000, v199
; __device__ __forceinline__ int q_i8(float v) { const int q = __float2int_rn(v); return q < -127 ? -127 : (q > 127 ? 127 : q); }
; __device__ __forceinline__ int pk_i8(float a, float b, float c, float d) { return (int)((unsigned)(q_i8(a) & 0xff) | ((unsigned)(q_i8(b) & 0xff) << 8) | ((unsigned)(q_i8(c) & 0xff) << 16) | ((unsigned)(q_i8(d) & 0xff) << 24)); }
	v_cndmask_b32_e32 v199, v199, v205, vcc
	v_cmp_class_f32_e32 vcc, v198, v200
	s_nop 1
	v_cndmask_b32_e32 v198, v199, v198, vcc
	v_div_scale_f32 v199, s[0:1], v198, v198, 1.0
	v_rcp_f32_e32 v205, v199
	s_nop 0
	v_fma_f32 v206, -v199, v205, 1.0
	v_fmac_f32_e32 v205, v206, v205
	v_div_scale_f32 v206, vcc, 1.0, v198, 1.0
	v_mul_f32_e32 v207, v206, v205
	v_fma_f32 v208, -v199, v207, v206
	v_fmac_f32_e32 v207, v208, v205
	v_fma_f32 v199, -v199, v207, v206
	v_div_fmas_f32 v199, v199, v205, v207
	v_div_fixup_f32 v198, v199, v198, 1.0
	v_mul_f32_e32 v199, v190, v198
	v_mul_f32_e32 v193, v193, v198
	v_mul_f32_e32 v190, v191, v198
	v_mul_f32_e32 v191, v192, v198
	v_mul_f32_e32 v192, v186, v198
	v_mul_f32_e32 v186, v187, v198
	v_mul_f32_e32 v187, v188, v198
	v_mul_f32_e32 v188, v182, v198
	v_mul_f32_e32 v182, v183, v198
	v_mul_f32_e32 v183, v184, v198
	v_mul_f32_e32 v184, v178, v198
	v_mul_f32_e32 v178, v179, v198
	v_mul_f32_e32 v179, v180, v198
	v_mul_f32_e32 v180, v174, v198
	v_mul_f32_e32 v174, v175, v198
	v_mul_f32_e32 v175, v176, v198
	v_mul_f32_e32 v176, v170, v198
	v_mul_f32_e32 v170, v171, v198
	v_mul_f32_e32 v171, v172, v198
	v_mul_f32_e32 v172, v162, v198
	v_mul_f32_e32 v162, v163, v198
	v_mul_f32_e32 v163, v164, v198
	v_mul_f32_e32 v205, v165, v198
	v_mul_f32_e32 v164, v167, v198
	v_mul_f32_e32 v165, v168, v198
	v_mul_f32_e32 v168, v169, v198
	v_mul_f32_e32 v167, v158, v198
	v_mul_f32_e32 v158, v159, v198
	v_mul_f32_e32 v159, v160, v198
	v_mul_f32_e32 v160, v154, v198
	v_mul_f32_e32 v154, v155, v198
	v_mul_f32_e32 v155, v156, v198
	v_mul_f32_e32 v156, v150, v198
	v_mul_f32_e32 v150, v151, v198
	v_mul_f32_e32 v151, v152, v198
	v_mul_f32_e32 v152, v153, v198
	v_mul_f32_e32 v153, v102, v198
	v_mul_f32_e32 v169, v103, v198
	v_mul_f32_e32 v102, v62, v199
	v_mul_f32_e32 v103, v65, v193
	v_mul_f32_e32 v102, 0x42000000, v102
	v_mul_f32_e32 v103, 0x42000000, v103
	v_rndne_f32_e32 v102, v102
	v_rndne_f32_e32 v103, v103
	v_cvt_i32_f32_e32 v102, v102
	v_cvt_i32_f32_e32 v103, v103
	v_mul_f32_e32 v189, v189, v198
	v_mul_f32_e32 v189, v61, v189
	v_med3_i32 v102, v102, s11, v204
	v_med3_i32 v103, v103, s11, v204
	v_perm_b32 v102, v103, v102, s19
	v_mul_f32_e32 v103, v63, v190
	v_mul_f32_e32 v190, v64, v191
	v_mul_f32_e32 v103, 0x42000000, v103
	v_mul_f32_e32 v190, 0x42000000, v190
	v_rndne_f32_e32 v103, v103
	v_rndne_f32_e32 v190, v190
	v_cvt_i32_f32_e32 v103, v103
	v_cvt_i32_f32_e32 v190, v190
	v_mul_f32_e32 v191, v58, v192
	v_mul_f32_e32 v191, 0x42000000, v191
	v_mul_f32_e32 v189, 0x42000000, v189
	v_rndne_f32_e32 v191, v191
	v_rndne_f32_e32 v189, v189
	v_cvt_i32_f32_e32 v191, v191
	v_cvt_i32_f32_e32 v189, v189
	v_med3_i32 v103, v103, s11, v204
	v_med3_i32 v190, v190, s11, v204
	v_lshlrev_b32_e32 v103, 8, v103
	v_lshlrev_b32_e32 v190, 16, v190
	v_and_b32_e32 v103, 0xff00, v103
	v_and_b32_e32 v190, 0xff0000, v190
	v_or3_b32 v190, v102, v103, v190
	v_med3_i32 v102, v191, s11, v204
	v_med3_i32 v103, v189, s11, v204
	v_perm_b32 v102, v103, v102, s19
	v_mul_f32_e32 v103, v59, v186
	v_mul_f32_e32 v186, v60, v187
	v_mul_f32_e32 v103, 0x42000000, v103
	v_mul_f32_e32 v186, 0x42000000, v186
	v_mul_f32_e32 v185, v185, v198
	v_rndne_f32_e32 v103, v103
	v_rndne_f32_e32 v186, v186
	v_cvt_i32_f32_e32 v103, v103
	v_cvt_i32_f32_e32 v186, v186
	v_mul_f32_e32 v187, v54, v188
	v_mul_f32_e32 v185, v57, v185
	v_mul_f32_e32 v187, 0x42000000, v187
	v_mul_f32_e32 v185, 0x42000000, v185
	v_rndne_f32_e32 v187, v187
	v_rndne_f32_e32 v185, v185
	v_cvt_i32_f32_e32 v187, v187
	v_cvt_i32_f32_e32 v185, v185
	v_med3_i32 v103, v103, s11, v204
	v_med3_i32 v186, v186, s11, v204
	v_lshlrev_b32_e32 v103, 8, v103
	v_lshlrev_b32_e32 v186, 16, v186
	v_and_b32_e32 v103, 0xff00, v103
	v_and_b32_e32 v186, 0xff0000, v186
	v_or3_b32 v186, v102, v103, v186
	v_med3_i32 v102, v187, s11, v204
	v_med3_i32 v103, v185, s11, v204
	v_perm_b32 v102, v103, v102, s19
	v_mul_f32_e32 v103, v55, v182
	v_mul_f32_e32 v182, v56, v183
	v_mul_f32_e32 v103, 0x42000000, v103
	v_mul_f32_e32 v182, 0x42000000, v182
	v_mul_f32_e32 v181, v181, v198
	v_rndne_f32_e32 v103, v103
	v_rndne_f32_e32 v182, v182
	v_cvt_i32_f32_e32 v103, v103
	v_cvt_i32_f32_e32 v182, v182
	v_mul_f32_e32 v183, v50, v184
	v_mul_f32_e32 v181, v53, v181
	v_mul_f32_e32 v183, 0x42000000, v183
	v_mul_f32_e32 v181, 0x42000000, v181
	v_rndne_f32_e32 v183, v183
	v_rndne_f32_e32 v181, v181
	v_cvt_i32_f32_e32 v183, v183
	v_cvt_i32_f32_e32 v181, v181
	v_med3_i32 v103, v103, s11, v204
	v_med3_i32 v182, v182, s11, v204
	v_lshlrev_b32_e32 v103, 8, v103
	v_lshlrev_b32_e32 v182, 16, v182
	v_and_b32_e32 v103, 0xff00, v103
	v_and_b32_e32 v182, 0xff0000, v182
	v_or3_b32 v182, v102, v103, v182
	v_med3_i32 v102, v183, s11, v204
	v_med3_i32 v103, v181, s11, v204
	v_perm_b32 v102, v103, v102, s19
	v_mul_f32_e32 v103, v51, v178
	v_mul_f32_e32 v178, v52, v179
	v_mul_f32_e32 v103, 0x42000000, v103
	v_mul_f32_e32 v178, 0x42000000, v178
	v_mul_f32_e32 v177, v177, v198
	v_rndne_f32_e32 v103, v103
	v_rndne_f32_e32 v178, v178
	v_cvt_i32_f32_e32 v103, v103
	v_cvt_i32_f32_e32 v178, v178
	v_mul_f32_e32 v179, v46, v180
	v_mul_f32_e32 v177, v49, v177
	v_mul_f32_e32 v179, 0x42000000, v179
	v_mul_f32_e32 v177, 0x42000000, v177
	v_rndne_f32_e32 v179, v179
	v_rndne_f32_e32 v177, v177
	v_cvt_i32_f32_e32 v179, v179
	v_cvt_i32_f32_e32 v177, v177
	v_med3_i32 v103, v103, s11, v204
	v_med3_i32 v178, v178, s11, v204
	v_lshlrev_b32_e32 v103, 8, v103
	v_lshlrev_b32_e32 v178, 16, v178
	v_and_b32_e32 v103, 0xff00, v103
	v_and_b32_e32 v178, 0xff0000, v178
	v_or3_b32 v178, v102, v103, v178
	v_med3_i32 v102, v179, s11, v204
	v_med3_i32 v103, v177, s11, v204
	v_perm_b32 v102, v103, v102, s19
; __device__ __forceinline__ int q_i8(float v) { const int q = __float2int_rn(v); return q < -127 ? -127 : (q > 127 ? 127 : q); }
; __device__ __forceinline__ int pk_i8(float a, float b, float c, float d) { return (int)((unsigned)(q_i8(a) & 0xff) | ((unsigned)(q_i8(b) & 0xff) << 8) | ((unsigned)(q_i8(c) & 0xff) << 16) | ((unsigned)(q_i8(d) & 0xff) << 24)); }
	v_mul_f32_e32 v103, v47, v174
	v_mul_f32_e32 v174, v48, v175
	v_mul_f32_e32 v103, 0x42000000, v103
	v_mul_f32_e32 v174, 0x42000000, v174
	v_mul_f32_e32 v173, v173, v198
	v_rndne_f32_e32 v103, v103
	v_rndne_f32_e32 v174, v174
	v_cvt_i32_f32_e32 v103, v103
	v_cvt_i32_f32_e32 v174, v174
	v_mul_f32_e32 v175, v42, v176
	v_mul_f32_e32 v173, v45, v173
	v_mul_f32_e32 v175, 0x42000000, v175
	v_mul_f32_e32 v173, 0x42000000, v173
	v_rndne_f32_e32 v175, v175
	v_rndne_f32_e32 v173, v173
	v_cvt_i32_f32_e32 v175, v175
	v_cvt_i32_f32_e32 v173, v173
	v_med3_i32 v103, v103, s11, v204
	v_med3_i32 v174, v174, s11, v204
	v_lshlrev_b32_e32 v103, 8, v103
	v_lshlrev_b32_e32 v174, 16, v174
	v_and_b32_e32 v103, 0xff00, v103
	v_and_b32_e32 v174, 0xff0000, v174
	v_or3_b32 v174, v102, v103, v174
	v_med3_i32 v102, v175, s11, v204
	v_med3_i32 v103, v173, s11, v204
	v_perm_b32 v102, v103, v102, s19
	v_mul_f32_e32 v103, v43, v170
	v_mul_f32_e32 v170, v44, v171
	v_mul_f32_e32 v103, 0x42000000, v103
	v_mul_f32_e32 v170, 0x42000000, v170
	v_rndne_f32_e32 v103, v103
	v_rndne_f32_e32 v170, v170
	v_cvt_i32_f32_e32 v103, v103
	v_cvt_i32_f32_e32 v170, v170
	v_mul_f32_e32 v171, v38, v172
	v_mul_f32_e32 v172, v41, v205
	v_mul_f32_e32 v171, 0x42000000, v171
	v_mul_f32_e32 v172, 0x42000000, v172
	v_rndne_f32_e32 v171, v171
	v_rndne_f32_e32 v172, v172
	v_cvt_i32_f32_e32 v171, v171
	v_cvt_i32_f32_e32 v172, v172
	v_med3_i32 v103, v103, s11, v204
	v_med3_i32 v170, v170, s11, v204
	v_lshlrev_b32_e32 v103, 8, v103
	v_lshlrev_b32_e32 v170, 16, v170
	v_and_b32_e32 v103, 0xff00, v103
	v_and_b32_e32 v170, 0xff0000, v170
	v_or3_b32 v170, v102, v103, v170
	v_med3_i32 v102, v171, s11, v204
	v_med3_i32 v103, v172, s11, v204
	v_perm_b32 v102, v103, v102, s19
	v_mul_f32_e32 v103, v39, v162
	v_mul_f32_e32 v162, v40, v163
	v_mul_f32_e32 v103, 0x42000000, v103
	v_mul_f32_e32 v162, 0x42000000, v162
	v_mul_f32_e32 v166, v166, v198
	v_rndne_f32_e32 v103, v103
	v_rndne_f32_e32 v162, v162
	v_cvt_i32_f32_e32 v103, v103
	v_cvt_i32_f32_e32 v162, v162
	v_mul_f32_e32 v163, v34, v166
	v_mul_f32_e32 v166, v37, v168
	v_mul_f32_e32 v163, 0x42000000, v163
	v_mul_f32_e32 v166, 0x42000000, v166
	v_rndne_f32_e32 v163, v163
	v_rndne_f32_e32 v166, v166
	v_cvt_i32_f32_e32 v163, v163
	v_cvt_i32_f32_e32 v166, v166
	v_med3_i32 v103, v103, s11, v204
	v_med3_i32 v162, v162, s11, v204
	v_lshlrev_b32_e32 v103, 8, v103
	v_lshlrev_b32_e32 v162, 16, v162
	v_and_b32_e32 v103, 0xff00, v103
	v_and_b32_e32 v162, 0xff0000, v162
	v_or3_b32 v162, v102, v103, v162
	v_med3_i32 v102, v163, s11, v204
	v_med3_i32 v103, v166, s11, v204
	v_perm_b32 v102, v103, v102, s19
	v_mul_f32_e32 v103, v35, v164
	v_mul_f32_e32 v163, v36, v165
	v_mul_f32_e32 v103, 0x42000000, v103
	v_mul_f32_e32 v163, 0x42000000, v163
	v_mul_f32_e32 v161, v161, v198
	v_rndne_f32_e32 v103, v103
	v_rndne_f32_e32 v163, v163
	v_cvt_i32_f32_e32 v103, v103
	v_cvt_i32_f32_e32 v163, v163
	v_mul_f32_e32 v164, v30, v167
	v_mul_f32_e32 v161, v33, v161
	v_mul_f32_e32 v164, 0x42000000, v164
	v_mul_f32_e32 v161, 0x42000000, v161
	v_rndne_f32_e32 v164, v164
	v_rndne_f32_e32 v161, v161
	v_cvt_i32_f32_e32 v164, v164
	v_cvt_i32_f32_e32 v161, v161
	v_med3_i32 v103, v103, s11, v204
	v_med3_i32 v163, v163, s11, v204
	v_lshlrev_b32_e32 v103, 8, v103
	v_lshlrev_b32_e32 v163, 16, v163
	v_and_b32_e32 v103, 0xff00, v103
	v_and_b32_e32 v163, 0xff0000, v163
	v_or3_b32 v163, v102, v103, v163
	v_med3_i32 v102, v164, s11, v204
	v_med3_i32 v103, v161, s11, v204
	v_perm_b32 v102, v103, v102, s19
	v_mul_f32_e32 v103, v31, v158
	v_mul_f32_e32 v158, v32, v159
	v_mul_f32_e32 v103, 0x42000000, v103
	v_mul_f32_e32 v158, 0x42000000, v158
	v_mul_f32_e32 v157, v157, v198
	v_rndne_f32_e32 v103, v103
	v_rndne_f32_e32 v158, v158
	v_cvt_i32_f32_e32 v103, v103
	v_cvt_i32_f32_e32 v158, v158
	v_mul_f32_e32 v159, v26, v160
	v_mul_f32_e32 v157, v29, v157
	v_mul_f32_e32 v159, 0x42000000, v159
	v_mul_f32_e32 v157, 0x42000000, v157
	v_rndne_f32_e32 v159, v159
	v_rndne_f32_e32 v157, v157
	v_cvt_i32_f32_e32 v159, v159
	v_cvt_i32_f32_e32 v157, v157
	v_med3_i32 v103, v103, s11, v204
	v_med3_i32 v158, v158, s11, v204
	v_lshlrev_b32_e32 v103, 8, v103
	v_lshlrev_b32_e32 v158, 16, v158
	v_and_b32_e32 v103, 0xff00, v103
	v_and_b32_e32 v158, 0xff0000, v158
	v_or3_b32 v158, v102, v103, v158
	v_med3_i32 v102, v159, s11, v204
	v_med3_i32 v103, v157, s11, v204
	v_perm_b32 v102, v103, v102, s19
	v_mul_f32_e32 v103, v27, v154
	v_mul_f32_e32 v154, v28, v155
	v_mul_f32_e32 v103, 0x42000000, v103
	v_mul_f32_e32 v154, 0x42000000, v154
	v_rndne_f32_e32 v103, v103
	v_rndne_f32_e32 v154, v154
	v_cvt_i32_f32_e32 v103, v103
	v_cvt_i32_f32_e32 v154, v154
	v_mul_f32_e32 v155, v22, v156
	v_mul_f32_e32 v152, v25, v152
	v_mul_f32_e32 v155, 0x42000000, v155
	v_mul_f32_e32 v152, 0x42000000, v152
	v_rndne_f32_e32 v155, v155
	v_rndne_f32_e32 v152, v152
	v_cvt_i32_f32_e32 v155, v155
	v_cvt_i32_f32_e32 v152, v152
	v_med3_i32 v103, v103, s11, v204
	v_med3_i32 v154, v154, s11, v204
	v_lshlrev_b32_e32 v103, 8, v103
	v_lshlrev_b32_e32 v154, 16, v154
	v_and_b32_e32 v103, 0xff00, v103
	v_and_b32_e32 v154, 0xff0000, v154
	v_or3_b32 v154, v102, v103, v154
	v_med3_i32 v102, v155, s11, v204
	v_med3_i32 v103, v152, s11, v204
	v_perm_b32 v102, v103, v102, s19
	v_mul_f32_e32 v103, v23, v150
	v_mul_f32_e32 v150, v24, v151
	v_mul_f32_e32 v103, 0x42000000, v103
	v_mul_f32_e32 v150, 0x42000000, v150
	v_mul_f32_e32 v110, v110, v198
	v_mul_f32_e32 v113, v113, v198
	v_rndne_f32_e32 v103, v103
	v_rndne_f32_e32 v150, v150
	v_cvt_i32_f32_e32 v103, v103
	v_cvt_i32_f32_e32 v150, v150
	v_mul_f32_e32 v110, v18, v110
	v_mul_f32_e32 v113, v21, v113
	v_mul_f32_e32 v110, 0x42000000, v110
; __device__ __forceinline__ int q_i8(float v) { const int q = __float2int_rn(v); return q < -127 ? -127 : (q > 127 ? 127 : q); }
; __device__ __forceinline__ int pk_i8(float a, float b, float c, float d) { return (int)((unsigned)(q_i8(a) & 0xff) | ((unsigned)(q_i8(b) & 0xff) << 8) | ((unsigned)(q_i8(c) & 0xff) << 16) | ((unsigned)(q_i8(d) & 0xff) << 24)); }
	v_mul_f32_e32 v113, 0x42000000, v113
	v_rndne_f32_e32 v110, v110
	v_rndne_f32_e32 v113, v113
	v_cvt_i32_f32_e32 v110, v110
	v_cvt_i32_f32_e32 v113, v113
	v_med3_i32 v103, v103, s11, v204
	v_med3_i32 v150, v150, s11, v204
	v_lshlrev_b32_e32 v103, 8, v103
	v_lshlrev_b32_e32 v150, 16, v150
	v_and_b32_e32 v103, 0xff00, v103
	v_and_b32_e32 v150, 0xff0000, v150
	v_mul_f32_e32 v111, v111, v198
	v_mul_f32_e32 v112, v112, v198
	v_or3_b32 v150, v102, v103, v150
	v_med3_i32 v102, v110, s11, v204
	v_med3_i32 v103, v113, s11, v204
	v_perm_b32 v102, v103, v102, s19
	v_mul_f32_e32 v103, v19, v111
	v_mul_f32_e32 v110, v20, v112
	v_mul_f32_e32 v103, 0x42000000, v103
	v_mul_f32_e32 v110, 0x42000000, v110
	v_rndne_f32_e32 v103, v103
	v_rndne_f32_e32 v110, v110
	v_cvt_i32_f32_e32 v103, v103
	v_cvt_i32_f32_e32 v110, v110
	v_mul_f32_e32 v104, v104, v198
	v_mul_f32_e32 v75, v75, v198
	v_med3_i32 v103, v103, s11, v204
	v_med3_i32 v110, v110, s11, v204
	v_lshlrev_b32_e32 v103, 8, v103
	v_lshlrev_b32_e32 v110, 16, v110
	v_and_b32_e32 v103, 0xff00, v103
	v_and_b32_e32 v110, 0xff0000, v110
	v_mul_f32_e32 v76, v76, v198
	v_mul_f32_e32 v71, v71, v198
	v_mul_f32_e32 v72, v72, v198
	v_mul_f32_e32 v67, v67, v198
	v_mul_f32_e32 v68, v68, v198
	v_mul_f32_e32 v105, v105, v198
	v_or3_b32 v110, v102, v103, v110
	v_mad_i64_i32 v[102:103], s[0:1], s21, v201, v[196:197]
	v_mul_f32_e32 v111, v15, v169
	v_mul_f32_e32 v104, v16, v104
	v_mul_f32_e32 v74, v74, v198
	v_mul_f32_e32 v75, v11, v75
	v_mul_f32_e32 v76, v12, v76
	v_mul_f32_e32 v77, v77, v198
	v_mul_f32_e32 v70, v70, v198
	v_mul_f32_e32 v71, v7, v71
	v_mul_f32_e32 v72, v8, v72
	v_mul_f32_e32 v73, v73, v198
	v_mul_f32_e32 v66, v66, v198
	v_mul_f32_e32 v67, v3, v67
	v_mul_f32_e32 v68, v4, v68
	v_mul_f32_e32 v69, v69, v198
	global_store_dword v[102:103], v190, off
	global_store_dword v[102:103], v186, off offset:256
	global_store_dword v[102:103], v182, off offset:512
	global_store_dword v[102:103], v178, off offset:768
	global_store_dword v[102:103], v174, off offset:1024
	global_store_dword v[102:103], v170, off offset:1280
	global_store_dword v[102:103], v162, off offset:1536
	global_store_dword v[102:103], v163, off offset:1792
	global_store_dword v[102:103], v158, off offset:2048
	global_store_dword v[102:103], v154, off offset:2304
	global_store_dword v[102:103], v150, off offset:2560
	global_store_dword v[102:103], v110, off offset:2816
	v_mul_f32_e32 v110, v14, v153
	v_mul_f32_e32 v105, v17, v105
	v_mul_f32_e32 v111, 0x42000000, v111
	v_mul_f32_e32 v104, 0x42000000, v104
	v_mul_f32_e32 v74, v10, v74
	v_mul_f32_e32 v77, v13, v77
	v_mul_f32_e32 v75, 0x42000000, v75
	v_mul_f32_e32 v76, 0x42000000, v76
	v_mul_f32_e32 v70, v6, v70
	v_mul_f32_e32 v73, v9, v73
	v_mul_f32_e32 v71, 0x42000000, v71
	v_mul_f32_e32 v72, 0x42000000, v72
	v_mul_f32_e32 v66, v2, v66
	v_mul_f32_e32 v69, v5, v69
	v_mul_f32_e32 v67, 0x42000000, v67
	v_mul_f32_e32 v68, 0x42000000, v68
	v_mul_f32_e32 v110, 0x42000000, v110
	v_rndne_f32_e32 v111, v111
	v_mul_f32_e32 v105, 0x42000000, v105
	v_rndne_f32_e32 v104, v104
	v_mul_f32_e32 v74, 0x42000000, v74
	v_rndne_f32_e32 v75, v75
	v_mul_f32_e32 v77, 0x42000000, v77
	v_rndne_f32_e32 v76, v76
	v_mul_f32_e32 v70, 0x42000000, v70
	v_rndne_f32_e32 v71, v71
	v_mul_f32_e32 v73, 0x42000000, v73
	v_rndne_f32_e32 v72, v72
	v_mul_f32_e32 v66, 0x42000000, v66
	v_rndne_f32_e32 v67, v67
	v_mul_f32_e32 v69, 0x42000000, v69
	v_rndne_f32_e32 v68, v68
	v_rndne_f32_e32 v110, v110
	v_cvt_i32_f32_e32 v111, v111
	v_cvt_i32_f32_e32 v104, v104
	v_rndne_f32_e32 v105, v105
	v_rndne_f32_e32 v74, v74
	v_cvt_i32_f32_e32 v75, v75
	v_cvt_i32_f32_e32 v76, v76
	v_rndne_f32_e32 v77, v77
	v_rndne_f32_e32 v70, v70
	v_cvt_i32_f32_e32 v71, v71
	v_cvt_i32_f32_e32 v72, v72
	v_rndne_f32_e32 v73, v73
	v_rndne_f32_e32 v66, v66
	v_cvt_i32_f32_e32 v67, v67
	v_cvt_i32_f32_e32 v68, v68
	v_rndne_f32_e32 v69, v69
	v_cvt_i32_f32_e32 v110, v110
	v_cvt_i32_f32_e32 v105, v105
	v_cvt_i32_f32_e32 v74, v74
	v_cvt_i32_f32_e32 v77, v77
	v_cvt_i32_f32_e32 v70, v70
	v_cvt_i32_f32_e32 v73, v73
	v_cvt_i32_f32_e32 v66, v66
	v_cvt_i32_f32_e32 v69, v69
	v_med3_i32 v111, v111, s11, v204
	v_med3_i32 v104, v104, s11, v204
	v_med3_i32 v75, v75, s11, v204
	v_med3_i32 v76, v76, s11, v204
	v_med3_i32 v71, v71, s11, v204
	v_med3_i32 v72, v72, s11, v204
	v_med3_i32 v67, v67, s11, v204
	v_med3_i32 v68, v68, s11, v204
	v_med3_i32 v110, v110, s11, v204
	v_lshlrev_b32_e32 v111, 8, v111
	v_lshlrev_b32_e32 v104, 16, v104
	v_med3_i32 v105, v105, s11, v204
	v_med3_i32 v74, v74, s11, v204
	v_lshlrev_b32_e32 v75, 8, v75
	v_lshlrev_b32_e32 v76, 16, v76
	v_med3_i32 v77, v77, s11, v204
	v_med3_i32 v70, v70, s11, v204
	v_lshlrev_b32_e32 v71, 8, v71
	v_lshlrev_b32_e32 v72, 16, v72
	v_med3_i32 v73, v73, s11, v204
	v_med3_i32 v66, v66, s11, v204
	v_lshlrev_b32_e32 v67, 8, v67
	v_lshlrev_b32_e32 v68, 16, v68
	v_med3_i32 v69, v69, s11, v204
	v_and_b32_e32 v111, 0xff00, v111
	v_and_b32_e32 v104, 0xff0000, v104
	v_perm_b32 v105, v105, v110, s19
	v_and_b32_e32 v75, 0xff00, v75
	v_and_b32_e32 v76, 0xff0000, v76
	v_perm_b32 v74, v77, v74, s19
	v_and_b32_e32 v71, 0xff00, v71
	v_and_b32_e32 v72, 0xff0000, v72
	v_perm_b32 v70, v73, v70, s19
	v_and_b32_e32 v67, 0xff00, v67
	v_and_b32_e32 v68, 0xff0000, v68
	v_perm_b32 v66, v69, v66, s19
	v_or3_b32 v104, v105, v111, v104
	v_or3_b32 v74, v74, v75, v76
	v_or3_b32 v70, v70, v71, v72
	v_or3_b32 v66, v66, v67, v68
	s_mov_b64 s[0:1], -1
	global_store_dword v[102:103], v104, off offset:3072
	global_store_dword v[102:103], v74, off offset:3328
	global_store_dword v[102:103], v70, off offset:3584
	global_store_dword v[102:103], v66, off offset:3840
	s_cbranch_scc1 .LBB0_94
; __device__ __forceinline__ float wave_sum(float v) {
;     v += __builtin_bit_cast(float, __builtin_amdgcn_update_dpp(0, __builtin_bit_cast(int, v), 0xB1, 0xf, 0xf, false));
;     v += __builtin_bit_cast(float, __builtin_amdgcn_update_dpp(0, __builtin_bit_cast(int, v), 0x4E, 0xf, 0xf, false));
;     v += __builtin_bit_cast(float, __builtin_amdgcn_update_dpp(0, __builtin_bit_cast(int, v), 0x141, 0xf, 0xf, false));
;     v += __builtin_bit_cast(float, __builtin_amdgcn_update_dpp(0, __builtin_bit_cast(int, v), 0x140, 0xf, 0xf, false));
;     { unsigned a_ = __builtin_bit_cast(unsigned, v), b_ = a_; asm volatile("" : "+v"(b_));
;       const auto r = __builtin_amdgcn_permlane16_swap(a_, b_, false, false); const unsigned r0_ = r[0], r1_ = r[1]; v = __uint_as_float(r0_) + __uint_as_float(r1_); }
;     { unsigned a_ = __builtin_bit_cast(unsigned, v), b_ = a_; asm volatile("" : "+v"(b_));
;       const auto r = __builtin_amdgcn_permlane32_swap(a_, b_, false, false); const unsigned r0_ = r[0], r1_ = r[1]; v = __uint_as_float(r0_) + __uint_as_float(r1_); }
;     return v;
	s_waitcnt vmcnt(31)
	v_mul_f32_e32 v198, v135, v135
	v_mul_f32_e32 v199, v137, v137
	v_fmac_f32_e32 v198, v134, v134
	v_fmac_f32_e32 v199, v136, v136
	v_add_f32_e32 v198, v198, v199
	s_waitcnt vmcnt(30)
	v_mul_f32_e32 v199, v127, v127
	v_mul_f32_e32 v205, v129, v129
	v_fmac_f32_e32 v199, v126, v126
	v_fmac_f32_e32 v205, v128, v128
	v_add_f32_e32 v199, v199, v205
	v_add_f32_e32 v198, v198, v199
	s_waitcnt vmcnt(29)
	v_mul_f32_e32 v199, v147, v147
	v_mul_f32_e32 v205, v149, v149
	v_fmac_f32_e32 v199, v146, v146
	v_fmac_f32_e32 v205, v148, v148
	v_add_f32_e32 v199, v199, v205
	v_add_f32_e32 v198, v198, v199
	s_waitcnt vmcnt(28)
	v_mul_f32_e32 v199, v143, v143
	v_mul_f32_e32 v205, v145, v145
	v_fmac_f32_e32 v199, v142, v142
	v_fmac_f32_e32 v205, v144, v144
	v_add_f32_e32 v199, v199, v205
	v_add_f32_e32 v198, v198, v199
	s_waitcnt vmcnt(17)
	v_mul_f32_e32 v199, v139, v139
	v_mul_f32_e32 v205, v141, v141
	v_fmac_f32_e32 v199, v138, v138
	v_fmac_f32_e32 v205, v140, v140
	v_add_f32_e32 v199, v199, v205
	v_add_f32_e32 v198, v198, v199
	v_mul_f32_e32 v199, v131, v131
	v_mul_f32_e32 v205, v133, v133
	v_fmac_f32_e32 v199, v130, v130
	v_fmac_f32_e32 v205, v132, v132
	v_add_f32_e32 v199, v199, v205
	v_add_f32_e32 v198, v198, v199
	v_mul_f32_e32 v199, v123, v123
	v_mul_f32_e32 v205, v125, v125
	v_fmac_f32_e32 v199, v122, v122
	v_fmac_f32_e32 v205, v124, v124
	v_add_f32_e32 v199, v199, v205
	v_add_f32_e32 v198, v198, v199
	v_mul_f32_e32 v199, v119, v119
	v_mul_f32_e32 v205, v121, v121
	v_fmac_f32_e32 v199, v118, v118
	v_fmac_f32_e32 v205, v120, v120
	v_add_f32_e32 v199, v199, v205
	v_add_f32_e32 v198, v198, v199
	v_mul_f32_e32 v199, v115, v115
	v_mul_f32_e32 v205, v117, v117
	v_fmac_f32_e32 v199, v114, v114
	v_fmac_f32_e32 v205, v116, v116
	v_add_f32_e32 v199, v199, v205
	v_add_f32_e32 v198, v198, v199
	v_mul_f32_e32 v199, v107, v107
	v_mul_f32_e32 v205, v109, v109
	v_fmac_f32_e32 v199, v106, v106
	v_fmac_f32_e32 v205, v108, v108
	v_add_f32_e32 v199, v199, v205
	v_add_f32_e32 v198, v198, v199
	v_mul_f32_e32 v199, v99, v99
	v_mul_f32_e32 v205, v101, v101
	v_fmac_f32_e32 v199, v98, v98
	v_fmac_f32_e32 v205, v100, v100
	v_add_f32_e32 v199, v199, v205
	v_add_f32_e32 v198, v198, v199
	v_mul_f32_e32 v199, v95, v95
	v_mul_f32_e32 v205, v97, v97
	v_fmac_f32_e32 v199, v94, v94
	v_fmac_f32_e32 v205, v96, v96
	v_add_f32_e32 v199, v199, v205
	v_add_f32_e32 v198, v198, v199
	v_mul_f32_e32 v199, v91, v91
	v_mul_f32_e32 v205, v93, v93
	v_fmac_f32_e32 v199, v90, v90
	v_fmac_f32_e32 v205, v92, v92
	v_add_f32_e32 v199, v199, v205
	v_add_f32_e32 v198, v198, v199
	v_mul_f32_e32 v199, v87, v87
	v_mul_f32_e32 v205, v89, v89
	v_fmac_f32_e32 v199, v86, v86
	v_fmac_f32_e32 v205, v88, v88
	v_add_f32_e32 v199, v199, v205
	s_add_i32 s22, s20, s33
	s_add_i32 s0, s7, s21
	v_add_f32_e32 v198, v198, v199
	v_mul_f32_e32 v199, v83, v83
	v_mul_f32_e32 v205, v85, v85
	s_cmpk_lt_i32 s0, 0x2000
	v_fmac_f32_e32 v199, v82, v82
	v_fmac_f32_e32 v205, v84, v84
	s_cselect_b32 s0, s0, s6
	v_add_f32_e32 v199, v199, v205
	s_ashr_i32 s1, s0, 31
	v_add_f32_e32 v198, v198, v199
	s_waitcnt vmcnt(16)
	v_mul_f32_e32 v199, v79, v79
	v_mul_f32_e32 v205, v81, v81
	s_lshl_b64 s[0:1], s[0:1], 14
	v_fmac_f32_e32 v199, v78, v78
	v_fmac_f32_e32 v205, v80, v80
	v_lshl_add_u64 v[66:67], v[194:195], 0, s[0:1]
	v_add_f32_e32 v199, v199, v205
	v_add_co_u32_e32 v68, vcc, 0x1000, v66
	v_add_f32_e32 v198, v198, v199
	s_nop 0
	v_addc_co_u32_e32 v69, vcc, 0, v67, vcc
	v_add_f32_dpp v198, v198, v198 quad_perm:[1,0,3,2] row_mask:0xf bank_mask:0xf bound_ctrl:1
	global_load_dwordx4 v[190:193], v[66:67], off nt
	global_load_dwordx4 v[186:189], v[66:67], off offset:1024 nt
	global_load_dwordx4 v[182:185], v[66:67], off offset:2048 nt
	global_load_dwordx4 v[178:181], v[66:67], off offset:3072 nt
	global_load_dwordx4 v[174:177], v[68:69], off nt
	global_load_dwordx4 v[170:173], v[68:69], off offset:1024 nt
	global_load_dwordx4 v[162:165], v[68:69], off offset:2048 nt
	global_load_dwordx4 v[166:169], v[68:69], off offset:3072 nt
	v_add_co_u32_e32 v68, vcc, s13, v66
	v_add_f32_dpp v198, v198, v198 quad_perm:[2,3,0,1] row_mask:0xf bank_mask:0xf bound_ctrl:1
	s_nop 0
	v_addc_co_u32_e32 v69, vcc, 0, v67, vcc
	v_add_f32_dpp v198, v198, v198 row_half_mirror row_mask:0xf bank_mask:0xf bound_ctrl:1
	v_add_co_u32_e32 v66, vcc, s12, v66
	s_nop 0
	v_add_f32_dpp v198, v198, v198 row_mirror row_mask:0xf bank_mask:0xf bound_ctrl:1
	v_addc_co_u32_e32 v67, vcc, 0, v67, vcc
	v_mov_b32_e32 v199, v198
	global_load_dwordx4 v[154:157], v[68:69], off offset:1024 nt
	global_load_dwordx4 v[150:153], v[68:69], off offset:2048 nt
	global_load_dwordx4 v[158:161], v[66:67], off offset:-4096 nt
	global_load_dwordx4 v[110:113], v[68:69], off offset:3072 nt
	global_load_dwordx4 v[102:105], v[66:67], off nt
	global_load_dwordx4 v[74:77], v[66:67], off offset:1024 nt
	global_load_dwordx4 v[70:73], v[66:67], off offset:2048 nt
	s_nop 0
	global_load_dwordx4 v[66:69], v[66:67], off offset:3072 nt
	s_cmpk_gt_i32 s22, 0x1fff
	v_permlane16_swap_b32_e32 v198, v199
	v_add_f32_e32 v198, v198, v199
	v_mov_b32_e32 v199, v198
	s_mov_b32 s21, s22
	s_nop 0
	v_permlane32_swap_b32_e32 v198, v199
	v_add_f32_e32 v198, v198, v199
	v_fmamk_f32 v198, v198, 0x39800000, v1
	v_mul_f32_e32 v199, 0x4f800000, v198
	v_cmp_gt_f32_e32 vcc, s10, v198
	s_nop 1
	v_cndmask_b32_e32 v198, v198, v199, vcc
	v_sqrt_f32_e32 v199, v198
	s_nop 0
	v_add_u32_e32 v205, -1, v199
	v_fma_f32 v206, -v205, v199, v198
	v_cmp_ge_f32_e64 s[0:1], 0, v206
	v_add_u32_e32 v206, 1, v199
	s_nop 0
	v_cndmask_b32_e64 v205, v199, v205, s[0:1]
	v_fma_f32 v199, -v206, v199, v198
	v_cmp_lt_f32_e64 s[0:1], 0, v199
	s_nop 1
; __device__ __forceinline__ int q_i8(float v) { const int q = __float2int_rn(v); return q < -127 ? -127 : (q > 127 ? 127 : q); }
; __device__ __forceinline__ int pk_i8(float a, float b, float c, float d) { return (int)((unsigned)(q_i8(a) & 0xff) | ((unsigned)(q_i8(b) & 0xff) << 8) | ((unsigned)(q_i8(c) & 0xff) << 16) | ((unsigned)(q_i8(d) & 0xff) << 24)); }
	v_cndmask_b32_e64 v199, v205, v206, s[0:1]
	v_mul_f32_e32 v205, 0x37800000, v199
	v_cndmask_b32_e32 v199, v199, v205, vcc
	v_cmp_class_f32_e32 vcc, v198, v200
	s_nop 1
	v_cndmask_b32_e32 v198, v199, v198, vcc
	v_div_scale_f32 v199, s[0:1], v198, v198, 1.0
	v_rcp_f32_e32 v205, v199
	s_nop 0
	v_fma_f32 v206, -v199, v205, 1.0
	v_fmac_f32_e32 v205, v206, v205
	v_div_scale_f32 v206, vcc, 1.0, v198, 1.0
	v_mul_f32_e32 v207, v206, v205
	v_fma_f32 v208, -v199, v207, v206
	v_fmac_f32_e32 v207, v208, v205
	v_fma_f32 v199, -v199, v207, v206
	v_div_fmas_f32 v199, v199, v205, v207
	v_div_fixup_f32 v205, v199, v198, 1.0
	v_mul_f32_e32 v127, v127, v205
	v_mul_f32_e32 v128, v128, v205
	v_mul_f32_e32 v126, v126, v205
	v_mul_f32_e32 v127, v59, v127
	v_mul_f32_e32 v128, v60, v128
	v_mul_f32_e32 v129, v129, v205
	v_mul_f32_e32 v126, v58, v126
	v_mul_f32_e32 v129, v61, v129
	v_mul_f32_e32 v127, 0x42000000, v127
	v_mul_f32_e32 v128, 0x42000000, v128
	v_mul_f32_e32 v126, 0x42000000, v126
	v_rndne_f32_e32 v127, v127
	v_mul_f32_e32 v129, 0x42000000, v129
	v_rndne_f32_e32 v128, v128
	v_rndne_f32_e32 v126, v126
	v_cvt_i32_f32_e32 v127, v127
	v_cvt_i32_f32_e32 v128, v128
	v_rndne_f32_e32 v129, v129
	v_cvt_i32_f32_e32 v126, v126
	v_cvt_i32_f32_e32 v129, v129
	v_med3_i32 v127, v127, s11, v204
	v_med3_i32 v128, v128, s11, v204
	v_med3_i32 v126, v126, s11, v204
	v_lshlrev_b32_e32 v127, 8, v127
	v_lshlrev_b32_e32 v128, 16, v128
	v_med3_i32 v129, v129, s11, v204
	v_and_b32_e32 v127, 0xff00, v127
	v_and_b32_e32 v128, 0xff0000, v128
	v_perm_b32 v126, v129, v126, s19
	v_mad_i64_i32 v[198:199], s[0:1], s20, v201, v[196:197]
	v_or3_b32 v126, v126, v127, v128
	v_mul_f32_e32 v127, v147, v205
	v_mul_f32_e32 v128, v148, v205
	global_store_dword v[198:199], v126, off offset:256
	v_mul_f32_e32 v126, v146, v205
	v_mul_f32_e32 v127, v55, v127
	v_mul_f32_e32 v128, v56, v128
	v_mul_f32_e32 v129, v149, v205
	v_mul_f32_e32 v126, v54, v126
	v_mul_f32_e32 v129, v57, v129
	v_mul_f32_e32 v127, 0x42000000, v127
	v_mul_f32_e32 v128, 0x42000000, v128
	v_mul_f32_e32 v126, 0x42000000, v126
	v_rndne_f32_e32 v127, v127
	v_mul_f32_e32 v129, 0x42000000, v129
	v_rndne_f32_e32 v128, v128
	v_rndne_f32_e32 v126, v126
	v_cvt_i32_f32_e32 v127, v127
	v_cvt_i32_f32_e32 v128, v128
	v_rndne_f32_e32 v129, v129
	v_cvt_i32_f32_e32 v126, v126
	v_cvt_i32_f32_e32 v129, v129
	v_med3_i32 v127, v127, s11, v204
	v_med3_i32 v128, v128, s11, v204
	v_med3_i32 v126, v126, s11, v204
	v_lshlrev_b32_e32 v127, 8, v127
	v_lshlrev_b32_e32 v128, 16, v128
	v_med3_i32 v129, v129, s11, v204
	v_and_b32_e32 v127, 0xff00, v127
	v_and_b32_e32 v128, 0xff0000, v128
	v_perm_b32 v126, v129, v126, s19
	v_or3_b32 v126, v126, v127, v128
	v_mul_f32_e32 v127, v143, v205
	v_mul_f32_e32 v128, v144, v205
	global_store_dword v[198:199], v126, off offset:512
	v_mul_f32_e32 v126, v142, v205
	v_mul_f32_e32 v127, v51, v127
	v_mul_f32_e32 v128, v52, v128
	v_mul_f32_e32 v129, v145, v205
	v_mul_f32_e32 v126, v50, v126
	v_mul_f32_e32 v129, v53, v129
	v_mul_f32_e32 v127, 0x42000000, v127
	v_mul_f32_e32 v128, 0x42000000, v128
	v_mul_f32_e32 v126, 0x42000000, v126
	v_rndne_f32_e32 v127, v127
	v_mul_f32_e32 v129, 0x42000000, v129
	v_rndne_f32_e32 v128, v128
	v_rndne_f32_e32 v126, v126
	v_cvt_i32_f32_e32 v127, v127
	v_cvt_i32_f32_e32 v128, v128
	v_rndne_f32_e32 v129, v129
	v_cvt_i32_f32_e32 v126, v126
	v_cvt_i32_f32_e32 v129, v129
	v_med3_i32 v127, v127, s11, v204
	v_med3_i32 v128, v128, s11, v204
	v_med3_i32 v126, v126, s11, v204
	v_lshlrev_b32_e32 v127, 8, v127
	v_lshlrev_b32_e32 v128, 16, v128
	v_med3_i32 v129, v129, s11, v204
	v_and_b32_e32 v127, 0xff00, v127
	v_and_b32_e32 v128, 0xff0000, v128
	v_perm_b32 v126, v129, v126, s19
	v_or3_b32 v126, v126, v127, v128
	v_mul_f32_e32 v127, v139, v205
	v_mul_f32_e32 v128, v140, v205
	global_store_dword v[198:199], v126, off offset:768
	v_mul_f32_e32 v126, v138, v205
	v_mul_f32_e32 v127, v47, v127
	v_mul_f32_e32 v128, v48, v128
	v_mul_f32_e32 v129, v141, v205
	v_mul_f32_e32 v126, v46, v126
	v_mul_f32_e32 v129, v49, v129
	v_mul_f32_e32 v127, 0x42000000, v127
	v_mul_f32_e32 v128, 0x42000000, v128
	v_mul_f32_e32 v126, 0x42000000, v126
	v_rndne_f32_e32 v127, v127
	v_mul_f32_e32 v129, 0x42000000, v129
	v_rndne_f32_e32 v128, v128
	v_rndne_f32_e32 v126, v126
	v_cvt_i32_f32_e32 v127, v127
	v_cvt_i32_f32_e32 v128, v128
	v_rndne_f32_e32 v129, v129
	v_cvt_i32_f32_e32 v126, v126
	v_cvt_i32_f32_e32 v129, v129
	v_med3_i32 v127, v127, s11, v204
	v_med3_i32 v128, v128, s11, v204
	v_med3_i32 v126, v126, s11, v204
	v_lshlrev_b32_e32 v127, 8, v127
	v_lshlrev_b32_e32 v128, 16, v128
	v_med3_i32 v129, v129, s11, v204
	v_and_b32_e32 v127, 0xff00, v127
	v_and_b32_e32 v128, 0xff0000, v128
	v_perm_b32 v126, v129, v126, s19
	v_mul_f32_e32 v135, v135, v205
	v_mul_f32_e32 v136, v136, v205
	v_or3_b32 v126, v126, v127, v128
	v_mul_f32_e32 v127, v131, v205
	v_mul_f32_e32 v128, v132, v205
	v_mul_f32_e32 v123, v123, v205
	v_mul_f32_e32 v124, v124, v205
	v_mul_f32_e32 v119, v119, v205
	v_mul_f32_e32 v120, v120, v205
	v_mul_f32_e32 v115, v115, v205
	v_mul_f32_e32 v116, v116, v205
	v_mul_f32_e32 v107, v107, v205
	v_mul_f32_e32 v108, v108, v205
	v_mul_f32_e32 v99, v99, v205
	v_mul_f32_e32 v100, v100, v205
	v_mul_f32_e32 v95, v95, v205
	v_mul_f32_e32 v96, v96, v205
	v_mul_f32_e32 v91, v91, v205
	v_mul_f32_e32 v92, v92, v205
	v_mul_f32_e32 v87, v87, v205
	v_mul_f32_e32 v88, v88, v205
	v_mul_f32_e32 v83, v83, v205
	v_mul_f32_e32 v84, v84, v205
	v_mul_f32_e32 v79, v79, v205
	v_mul_f32_e32 v80, v80, v205
	v_mul_f32_e32 v134, v134, v205
	v_mul_f32_e32 v135, v63, v135
	v_mul_f32_e32 v136, v64, v136
	v_mul_f32_e32 v137, v137, v205
	global_store_dword v[198:199], v126, off offset:1024
	v_mul_f32_e32 v126, v130, v205
	v_mul_f32_e32 v127, v43, v127
	v_mul_f32_e32 v128, v44, v128
	v_mul_f32_e32 v129, v133, v205
	v_mul_f32_e32 v122, v122, v205
	v_mul_f32_e32 v123, v39, v123
	v_mul_f32_e32 v124, v40, v124
	v_mul_f32_e32 v125, v125, v205
	v_mul_f32_e32 v118, v118, v205
	v_mul_f32_e32 v119, v35, v119
	v_mul_f32_e32 v120, v36, v120
	v_mul_f32_e32 v121, v121, v205
	v_mul_f32_e32 v114, v114, v205
	v_mul_f32_e32 v115, v31, v115
	v_mul_f32_e32 v116, v32, v116
	v_mul_f32_e32 v117, v117, v205
	v_mul_f32_e32 v106, v106, v205
	v_mul_f32_e32 v107, v27, v107
	v_mul_f32_e32 v108, v28, v108
	v_mul_f32_e32 v109, v109, v205
	v_mul_f32_e32 v98, v98, v205
	v_mul_f32_e32 v99, v23, v99
	v_mul_f32_e32 v100, v24, v100
	v_mul_f32_e32 v101, v101, v205
	v_mul_f32_e32 v94, v94, v205
	v_mul_f32_e32 v95, v19, v95
	v_mul_f32_e32 v96, v20, v96
	v_mul_f32_e32 v97, v97, v205
	v_mul_f32_e32 v90, v90, v205
	v_mul_f32_e32 v91, v15, v91
	v_mul_f32_e32 v92, v16, v92
	v_mul_f32_e32 v93, v93, v205
	v_mul_f32_e32 v86, v86, v205
	v_mul_f32_e32 v87, v11, v87
	v_mul_f32_e32 v88, v12, v88
	v_mul_f32_e32 v89, v89, v205
	v_mul_f32_e32 v82, v82, v205
	v_mul_f32_e32 v83, v7, v83
	v_mul_f32_e32 v84, v8, v84
	v_mul_f32_e32 v85, v85, v205
	v_mul_f32_e32 v78, v78, v205
	v_mul_f32_e32 v79, v3, v79
	v_mul_f32_e32 v80, v4, v80
	v_mul_f32_e32 v81, v81, v205
	v_mul_f32_e32 v134, v62, v134
	v_mul_f32_e32 v137, v65, v137
	v_mul_f32_e32 v135, 0x42000000, v135
	v_mul_f32_e32 v136, 0x42000000, v136
	v_mul_f32_e32 v126, v42, v126
	v_mul_f32_e32 v129, v45, v129
	v_mul_f32_e32 v127, 0x42000000, v127
	v_mul_f32_e32 v128, 0x42000000, v128
	v_mul_f32_e32 v122, v38, v122
	v_mul_f32_e32 v125, v41, v125
	v_mul_f32_e32 v123, 0x42000000, v123
	v_mul_f32_e32 v124, 0x42000000, v124
	v_mul_f32_e32 v118, v34, v118
	v_mul_f32_e32 v121, v37, v121
	v_mul_f32_e32 v119, 0x42000000, v119
	v_mul_f32_e32 v120, 0x42000000, v120
	v_mul_f32_e32 v114, v30, v114
	v_mul_f32_e32 v117, v33, v117
	v_mul_f32_e32 v115, 0x42000000, v115
	v_mul_f32_e32 v116, 0x42000000, v116
	v_mul_f32_e32 v106, v26, v106
	v_mul_f32_e32 v109, v29, v109
	v_mul_f32_e32 v107, 0x42000000, v107
	v_mul_f32_e32 v108, 0x42000000, v108
	v_mul_f32_e32 v98, v22, v98
	v_mul_f32_e32 v101, v25, v101
	v_mul_f32_e32 v99, 0x42000000, v99
	v_mul_f32_e32 v100, 0x42000000, v100
	v_mul_f32_e32 v94, v18, v94
	v_mul_f32_e32 v97, v21, v97
	v_mul_f32_e32 v95, 0x42000000, v95
	v_mul_f32_e32 v96, 0x42000000, v96
	v_mul_f32_e32 v90, v14, v90
	v_mul_f32_e32 v93, v17, v93
	v_mul_f32_e32 v91, 0x42000000, v91
	v_mul_f32_e32 v92, 0x42000000, v92
	v_mul_f32_e32 v86, v10, v86
	v_mul_f32_e32 v89, v13, v89
	v_mul_f32_e32 v87, 0x42000000, v87
	v_mul_f32_e32 v88, 0x42000000, v88
	v_mul_f32_e32 v82, v6, v82
	v_mul_f32_e32 v85, v9, v85
	v_mul_f32_e32 v83, 0x42000000, v83
	v_mul_f32_e32 v84, 0x42000000, v84
	v_mul_f32_e32 v78, v2, v78
	v_mul_f32_e32 v81, v5, v81
	v_mul_f32_e32 v79, 0x42000000, v79
	v_mul_f32_e32 v80, 0x42000000, v80
	v_mul_f32_e32 v134, 0x42000000, v134
	v_rndne_f32_e32 v135, v135
	v_mul_f32_e32 v137, 0x42000000, v137
	v_rndne_f32_e32 v136, v136
	v_mul_f32_e32 v126, 0x42000000, v126
	v_rndne_f32_e32 v127, v127
	v_mul_f32_e32 v129, 0x42000000, v129
	v_rndne_f32_e32 v128, v128
	v_mul_f32_e32 v122, 0x42000000, v122
	v_rndne_f32_e32 v123, v123
	v_mul_f32_e32 v125, 0x42000000, v125
	v_rndne_f32_e32 v124, v124
	v_mul_f32_e32 v118, 0x42000000, v118
	v_rndne_f32_e32 v119, v119
	v_mul_f32_e32 v121, 0x42000000, v121
	v_rndne_f32_e32 v120, v120
	v_mul_f32_e32 v114, 0x42000000, v114
	v_rndne_f32_e32 v115, v115
	v_mul_f32_e32 v117, 0x42000000, v117
	v_rndne_f32_e32 v116, v116
	v_mul_f32_e32 v106, 0x42000000, v106
	v_rndne_f32_e32 v107, v107
	v_mul_f32_e32 v109, 0x42000000, v109
	v_rndne_f32_e32 v108, v108
	v_mul_f32_e32 v98, 0x42000000, v98
	v_rndne_f32_e32 v99, v99
	v_mul_f32_e32 v101, 0x42000000, v101
	v_rndne_f32_e32 v100, v100
	v_mul_f32_e32 v94, 0x42000000, v94
	v_rndne_f32_e32 v95, v95
	v_mul_f32_e32 v97, 0x42000000, v97
	v_rndne_f32_e32 v96, v96
	v_mul_f32_e32 v90, 0x42000000, v90
	v_rndne_f32_e32 v91, v91
	v_mul_f32_e32 v93, 0x42000000, v93
	v_rndne_f32_e32 v92, v92
	v_mul_f32_e32 v86, 0x42000000, v86
	v_rndne_f32_e32 v87, v87
	v_mul_f32_e32 v89, 0x42000000, v89
	v_rndne_f32_e32 v88, v88
	v_mul_f32_e32 v82, 0x42000000, v82
	v_rndne_f32_e32 v83, v83
	v_mul_f32_e32 v85, 0x42000000, v85
	v_rndne_f32_e32 v84, v84
	v_mul_f32_e32 v78, 0x42000000, v78
	v_rndne_f32_e32 v79, v79
	v_mul_f32_e32 v81, 0x42000000, v81
	v_rndne_f32_e32 v80, v80
	v_rndne_f32_e32 v134, v134
	v_cvt_i32_f32_e32 v135, v135
	v_cvt_i32_f32_e32 v136, v136
	v_rndne_f32_e32 v137, v137
	v_rndne_f32_e32 v126, v126
	v_cvt_i32_f32_e32 v127, v127
	v_cvt_i32_f32_e32 v128, v128
	v_rndne_f32_e32 v129, v129
	v_rndne_f32_e32 v122, v122
	v_cvt_i32_f32_e32 v123, v123
	v_cvt_i32_f32_e32 v124, v124
	v_rndne_f32_e32 v125, v125
	v_rndne_f32_e32 v118, v118
	v_cvt_i32_f32_e32 v119, v119
	v_cvt_i32_f32_e32 v120, v120
	v_rndne_f32_e32 v121, v121
	v_rndne_f32_e32 v114, v114
	v_cvt_i32_f32_e32 v115, v115
	v_cvt_i32_f32_e32 v116, v116
	v_rndne_f32_e32 v117, v117
	v_rndne_f32_e32 v106, v106
	v_cvt_i32_f32_e32 v107, v107
	v_cvt_i32_f32_e32 v108, v108
	v_rndne_f32_e32 v109, v109
	v_rndne_f32_e32 v98, v98
	v_cvt_i32_f32_e32 v99, v99
	v_cvt_i32_f32_e32 v100, v100
	v_rndne_f32_e32 v101, v101
	v_rndne_f32_e32 v94, v94
	v_cvt_i32_f32_e32 v95, v95
	v_cvt_i32_f32_e32 v96, v96
	v_rndne_f32_e32 v97, v97
	v_rndne_f32_e32 v90, v90
	v_cvt_i32_f32_e32 v91, v91
	v_cvt_i32_f32_e32 v92, v92
	v_rndne_f32_e32 v93, v93
	v_rndne_f32_e32 v86, v86
	v_cvt_i32_f32_e32 v87, v87
	v_cvt_i32_f32_e32 v88, v88
; __device__ __forceinline__ int q_i8(float v) { const int q = __float2int_rn(v); return q < -127 ? -127 : (q > 127 ? 127 : q); }
; __device__ __forceinline__ int pk_i8(float a, float b, float c, float d) { return (int)((unsigned)(q_i8(a) & 0xff) | ((unsigned)(q_i8(b) & 0xff) << 8) | ((unsigned)(q_i8(c) & 0xff) << 16) | ((unsigned)(q_i8(d) & 0xff) << 24)); }
	v_rndne_f32_e32 v89, v89
	v_rndne_f32_e32 v82, v82
	v_cvt_i32_f32_e32 v83, v83
	v_cvt_i32_f32_e32 v84, v84
	v_rndne_f32_e32 v85, v85
	v_rndne_f32_e32 v78, v78
	v_cvt_i32_f32_e32 v79, v79
	v_cvt_i32_f32_e32 v80, v80
	v_rndne_f32_e32 v81, v81
	v_cvt_i32_f32_e32 v134, v134
	v_cvt_i32_f32_e32 v137, v137
	v_cvt_i32_f32_e32 v126, v126
	v_cvt_i32_f32_e32 v129, v129
	v_cvt_i32_f32_e32 v122, v122
	v_cvt_i32_f32_e32 v125, v125
	v_cvt_i32_f32_e32 v118, v118
	v_cvt_i32_f32_e32 v121, v121
	v_cvt_i32_f32_e32 v114, v114
	v_cvt_i32_f32_e32 v117, v117
	v_cvt_i32_f32_e32 v106, v106
	v_cvt_i32_f32_e32 v109, v109
	v_cvt_i32_f32_e32 v98, v98
	v_cvt_i32_f32_e32 v101, v101
	v_cvt_i32_f32_e32 v94, v94
	v_cvt_i32_f32_e32 v97, v97
	v_cvt_i32_f32_e32 v90, v90
	v_cvt_i32_f32_e32 v93, v93
	v_cvt_i32_f32_e32 v86, v86
	v_cvt_i32_f32_e32 v89, v89
	v_cvt_i32_f32_e32 v82, v82
	v_cvt_i32_f32_e32 v85, v85
	v_cvt_i32_f32_e32 v78, v78
	v_cvt_i32_f32_e32 v81, v81
	v_med3_i32 v135, v135, s11, v204
	v_med3_i32 v136, v136, s11, v204
	v_med3_i32 v127, v127, s11, v204
	v_med3_i32 v128, v128, s11, v204
	v_med3_i32 v123, v123, s11, v204
	v_med3_i32 v124, v124, s11, v204
	v_med3_i32 v119, v119, s11, v204
	v_med3_i32 v120, v120, s11, v204
	v_med3_i32 v115, v115, s11, v204
	v_med3_i32 v116, v116, s11, v204
	v_med3_i32 v107, v107, s11, v204
	v_med3_i32 v108, v108, s11, v204
	v_med3_i32 v99, v99, s11, v204
	v_med3_i32 v100, v100, s11, v204
	v_med3_i32 v95, v95, s11, v204
	v_med3_i32 v96, v96, s11, v204
	v_med3_i32 v91, v91, s11, v204
	v_med3_i32 v92, v92, s11, v204
	v_med3_i32 v87, v87, s11, v204
	v_med3_i32 v88, v88, s11, v204
	v_med3_i32 v83, v83, s11, v204
	v_med3_i32 v84, v84, s11, v204
	v_med3_i32 v79, v79, s11, v204
	v_med3_i32 v80, v80, s11, v204
	v_med3_i32 v134, v134, s11, v204
	v_lshlrev_b32_e32 v135, 8, v135
	v_lshlrev_b32_e32 v136, 16, v136
	v_med3_i32 v137, v137, s11, v204
	v_med3_i32 v126, v126, s11, v204
	v_lshlrev_b32_e32 v127, 8, v127
	v_lshlrev_b32_e32 v128, 16, v128
	v_med3_i32 v129, v129, s11, v204
	v_med3_i32 v122, v122, s11, v204
	v_lshlrev_b32_e32 v123, 8, v123
	v_lshlrev_b32_e32 v124, 16, v124
	v_med3_i32 v125, v125, s11, v204
	v_med3_i32 v118, v118, s11, v204
	v_lshlrev_b32_e32 v119, 8, v119
	v_lshlrev_b32_e32 v120, 16, v120
	v_med3_i32 v121, v121, s11, v204
	v_med3_i32 v114, v114, s11, v204
	v_lshlrev_b32_e32 v115, 8, v115
	v_lshlrev_b32_e32 v116, 16, v116
	v_med3_i32 v117, v117, s11, v204
	v_med3_i32 v106, v106, s11, v204
	v_lshlrev_b32_e32 v107, 8, v107
	v_lshlrev_b32_e32 v108, 16, v108
	v_med3_i32 v109, v109, s11, v204
	v_med3_i32 v98, v98, s11, v204
	v_lshlrev_b32_e32 v99, 8, v99
	v_lshlrev_b32_e32 v100, 16, v100
	v_med3_i32 v101, v101, s11, v204
	v_med3_i32 v94, v94, s11, v204
	v_lshlrev_b32_e32 v95, 8, v95
	v_lshlrev_b32_e32 v96, 16, v96
	v_med3_i32 v97, v97, s11, v204
	v_med3_i32 v90, v90, s11, v204
	v_lshlrev_b32_e32 v91, 8, v91
	v_lshlrev_b32_e32 v92, 16, v92
	v_med3_i32 v93, v93, s11, v204
	v_med3_i32 v86, v86, s11, v204
	v_lshlrev_b32_e32 v87, 8, v87
	v_lshlrev_b32_e32 v88, 16, v88
	v_med3_i32 v89, v89, s11, v204
	v_med3_i32 v82, v82, s11, v204
	v_lshlrev_b32_e32 v83, 8, v83
	v_lshlrev_b32_e32 v84, 16, v84
	v_med3_i32 v85, v85, s11, v204
	v_med3_i32 v78, v78, s11, v204
	v_lshlrev_b32_e32 v79, 8, v79
	v_lshlrev_b32_e32 v80, 16, v80
	v_med3_i32 v81, v81, s11, v204
	v_and_b32_e32 v135, 0xff00, v135
	v_and_b32_e32 v136, 0xff0000, v136
	v_perm_b32 v134, v137, v134, s19
	v_and_b32_e32 v127, 0xff00, v127
	v_and_b32_e32 v128, 0xff0000, v128
	v_perm_b32 v126, v129, v126, s19
	v_and_b32_e32 v123, 0xff00, v123
	v_and_b32_e32 v124, 0xff0000, v124
	v_perm_b32 v122, v125, v122, s19
	v_and_b32_e32 v119, 0xff00, v119
	v_and_b32_e32 v120, 0xff0000, v120
	v_perm_b32 v118, v121, v118, s19
	v_and_b32_e32 v115, 0xff00, v115
	v_and_b32_e32 v116, 0xff0000, v116
	v_perm_b32 v114, v117, v114, s19
	v_and_b32_e32 v107, 0xff00, v107
	v_and_b32_e32 v108, 0xff0000, v108
	v_perm_b32 v106, v109, v106, s19
	v_and_b32_e32 v99, 0xff00, v99
	v_and_b32_e32 v100, 0xff0000, v100
	v_perm_b32 v98, v101, v98, s19
	v_and_b32_e32 v95, 0xff00, v95
	v_and_b32_e32 v96, 0xff0000, v96
	v_perm_b32 v94, v97, v94, s19
	v_and_b32_e32 v91, 0xff00, v91
	v_and_b32_e32 v92, 0xff0000, v92
	v_perm_b32 v90, v93, v90, s19
	v_and_b32_e32 v87, 0xff00, v87
	v_and_b32_e32 v88, 0xff0000, v88
	v_perm_b32 v86, v89, v86, s19
	v_and_b32_e32 v83, 0xff00, v83
	v_and_b32_e32 v84, 0xff0000, v84
	v_perm_b32 v82, v85, v82, s19
	v_and_b32_e32 v79, 0xff00, v79
	v_and_b32_e32 v80, 0xff0000, v80
	v_perm_b32 v78, v81, v78, s19
	v_or3_b32 v134, v134, v135, v136
	v_or3_b32 v126, v126, v127, v128
	v_or3_b32 v122, v122, v123, v124
	v_or3_b32 v118, v118, v119, v120
	v_or3_b32 v114, v114, v115, v116
	v_or3_b32 v106, v106, v107, v108
	v_or3_b32 v98, v98, v99, v100
	v_or3_b32 v94, v94, v95, v96
	v_or3_b32 v90, v90, v91, v92
	v_or3_b32 v86, v86, v87, v88
	v_or3_b32 v82, v82, v83, v84
	v_or3_b32 v78, v78, v79, v80
	s_cselect_b64 s[0:1], -1, 0
	global_store_dword v[198:199], v134, off
	global_store_dword v[198:199], v126, off offset:1280
	global_store_dword v[198:199], v122, off offset:1536
	global_store_dword v[198:199], v118, off offset:1792
	global_store_dword v[198:199], v114, off offset:2048
	global_store_dword v[198:199], v106, off offset:2304
	global_store_dword v[198:199], v98, off offset:2560
	global_store_dword v[198:199], v94, off offset:2816
	global_store_dword v[198:199], v90, off offset:3072
	global_store_dword v[198:199], v86, off offset:3328
	global_store_dword v[198:199], v82, off offset:3584
	global_store_dword v[198:199], v78, off offset:3840
	s_branch .LBB0_94
